# write-through (sc1) output stores in wconv, LN and retention kernels; 4-phase GEMM K-loops
# speedup vs baseline: 1.0223x; 1.0051x over previous
_Z12wconv_kernel5WDesci:
	s_load_dword s4, s[0:1], 0x150
	s_waitcnt lgkmcnt(0)
	s_add_i32 s4, s4, s3
	s_ashr_i32 s5, s4, 31
	s_lshl_b64 s[4:5], s[4:5], 2
	s_add_u32 s0, s0, s4
	s_addc_u32 s1, s1, s5
	s_load_dword s7, s[0:1], 0x118
	s_load_dword s6, s[0:1], 0xe0
	s_waitcnt lgkmcnt(0)
	s_ashr_i32 s3, s7, 6
	v_cvt_f32_u32_e32 v1, s3
	s_sub_i32 s8, 0, s3
	v_rcp_iflag_f32_e32 v1, v1
	s_nop 0
	v_mul_f32_e32 v1, 0x4f7ffffe, v1
	v_cvt_u32_f32_e32 v1, v1
	s_nop 0
	v_readfirstlane_b32 s9, v1
	s_mul_i32 s8, s8, s9
	s_mul_hi_u32 s8, s9, s8
	s_add_i32 s9, s9, s8
	s_mul_hi_u32 s8, s2, s9
	s_mul_i32 s9, s8, s3
	s_sub_i32 s9, s2, s9
	s_add_i32 s10, s8, 1
	s_sub_i32 s11, s9, s3
	s_cmp_ge_u32 s9, s3
	s_cselect_b32 s8, s10, s8
	s_cselect_b32 s9, s11, s9
	s_add_i32 s10, s8, 1
	s_cmp_ge_u32 s9, s3
	s_cselect_b32 s8, s10, s8
	s_ashr_i32 s9, s6, 6
	s_cmp_ge_i32 s8, s9
	s_cbranch_scc1 .LBB0_2
	s_mul_i32 s3, s8, s3
	s_sub_i32 s2, s2, s3
	s_add_u32 s4, s0, s4
	s_addc_u32 s5, s1, s5
	s_load_dwordx2 s[10:11], s[4:5], 0x0
	s_lshl_b32 s2, s2, 6
	s_ashr_i32 s3, s2, 31
	s_lshl_b32 s0, s8, 6
	s_lshl_b64 s[8:9], s[2:3], 2
	v_lshrrev_b32_e32 v1, 4, v0
	s_waitcnt lgkmcnt(0)
	s_add_u32 s8, s10, s8
	v_lshlrev_b32_e32 v2, 4, v0
	s_addc_u32 s9, s11, s9
	v_and_b32_e32 v18, 0xf0, v2
	v_mov_b32_e32 v19, 0
	v_or_b32_e32 v16, s0, v1
	v_lshl_add_u64 v[14:15], s[8:9], 0, v[18:19]
	v_mad_i64_i32 v[2:3], s[8:9], v16, s7, 0
	v_lshl_add_u64 v[10:11], v[2:3], 2, v[14:15]
	v_or_b32_e32 v2, 16, v16
	v_mad_i64_i32 v[2:3], s[8:9], v2, s7, 0
	v_lshl_add_u64 v[12:13], v[2:3], 2, v[14:15]
	global_load_dwordx4 v[2:5], v[10:11], off nt
	global_load_dwordx4 v[6:9], v[12:13], off nt
	v_or_b32_e32 v10, 32, v16
	v_mad_i64_i32 v[10:11], s[8:9], v10, s7, 0
	v_lshl_add_u64 v[10:11], v[10:11], 2, v[14:15]
	v_or_b32_e32 v16, 48, v16
	global_load_dwordx4 v[10:13], v[10:11], off nt
	v_mad_i64_i32 v[16:17], s[8:9], v16, s7, 0
	v_lshl_add_u64 v[14:15], v[16:17], 2, v[14:15]
	global_load_dwordx4 v[14:17], v[14:15], off nt
	s_load_dwordx2 s[4:5], s[4:5], 0x70
	v_lshrrev_b32_e32 v20, 3, v0
	v_lshlrev_b32_e32 v0, 3, v0
	s_movk_i32 s1, 0x104
	v_and_b32_e32 v22, 56, v0
	v_lshlrev_b32_e32 v0, 2, v20
	v_mad_u32_u24 v24, v1, s1, v18
	v_mad_u32_u24 v25, v22, s1, v0
	v_add_u32_e32 v26, 0x1040, v24
	v_add_u32_e32 v27, 0x1048, v24
	v_add_u32_e32 v28, 0x2080, v24
	v_add_u32_e32 v29, 0x2088, v24
	v_add_u32_e32 v30, 0x30c0, v24
	v_add_u32_e32 v31, 0x30c8, v24
	v_add_u32_e32 v32, 0x400, v25
	s_ashr_i32 s1, s0, 31
	v_or_b32_e32 v18, s2, v20
	s_lshl_b64 s[0:1], s[0:1], 1
	v_mad_i64_i32 v[0:1], s[2:3], v18, s6, 0
	v_or_b32_e32 v18, 32, v18
	s_waitcnt lgkmcnt(0)
	s_add_u32 s0, s4, s0
	v_mad_i64_i32 v[20:21], s[2:3], v18, s6, 0
	v_lshlrev_b32_e32 v18, 1, v22
	s_addc_u32 s1, s5, s1
	v_lshl_add_u64 v[18:19], s[0:1], 0, v[18:19]
	v_lshl_add_u64 v[22:23], v[0:1], 1, v[18:19]
	v_lshl_add_u64 v[18:19], v[20:21], 1, v[18:19]
	s_waitcnt vmcnt(3)
	ds_write2_b32 v24, v2, v3 offset1:1
	ds_write2_b32 v24, v4, v5 offset0:2 offset1:3
	s_waitcnt vmcnt(2)
	ds_write2_b32 v26, v6, v7 offset1:1
	ds_write2_b32 v27, v8, v9 offset1:1
	s_waitcnt vmcnt(1)
	ds_write2_b32 v28, v10, v11 offset1:1
	ds_write2_b32 v29, v12, v13 offset1:1
	s_waitcnt vmcnt(0)
	ds_write2_b32 v30, v14, v15 offset1:1
	ds_write2_b32 v31, v16, v17 offset1:1
	s_waitcnt lgkmcnt(0)
	s_barrier
	ds_read2_b32 v[8:9], v25 offset1:32
	ds_read2_b32 v[4:5], v25 offset0:130 offset1:162
	ds_read2_b32 v[10:11], v32 offset0:4 offset1:36
	ds_read2_b32 v[6:7], v32 offset0:134 offset1:166
	ds_read2_b32 v[12:13], v32 offset0:199 offset1:231
	ds_read2_b32 v[14:15], v32 offset0:69 offset1:101
	ds_read2_b32 v[16:17], v25 offset0:195 offset1:227
	ds_read2_b32 v[24:25], v25 offset0:65 offset1:97
	s_waitcnt lgkmcnt(3)
	v_cvt_pk_f16_f32 v3, v6, v12
	s_waitcnt lgkmcnt(2)
	v_cvt_pk_f16_f32 v2, v10, v14
	s_waitcnt lgkmcnt(1)
	v_cvt_pk_f16_f32 v1, v4, v16
	s_waitcnt lgkmcnt(0)
	v_cvt_pk_f16_f32 v0, v8, v24
	v_cvt_pk_f16_f32 v7, v7, v13
	v_cvt_pk_f16_f32 v6, v11, v15
	v_cvt_pk_f16_f32 v5, v5, v17
	v_cvt_pk_f16_f32 v4, v9, v25
	global_store_dwordx4 v[22:23], v[0:3], off sc1
	global_store_dwordx4 v[18:19], v[4:7], off sc1

.LBB1_26:
	v_lshlrev_b32_e32 v0, 4, v141
	s_or_b32 s0, s33, s71
	v_add3_u32 v0, v140, v0, s0
	v_mov_b32_e32 v1, 0
	v_lshlrev_b64 v[8:9], 11, v[0:1]
	v_or_b32_e32 v0, s70, v8
	v_lshl_or_b32 v8, v156, 2, v0
	v_lshlrev_b64 v[60:61], 1, v[8:9]
	v_lshl_add_u64 v[30:31], s[42:43], 0, v[60:61]
	s_movk_i32 s18, 0x2000
	v_add_co_u32_e32 v34, vcc, s18, v30
	s_movk_i32 s17, 0x4000
	s_nop 0
	v_addc_co_u32_e32 v35, vcc, 0, v31, vcc
	s_lshl_b32 s2, s70, 2
	v_add_co_u32_e32 v8, vcc, s17, v30
	s_waitcnt lgkmcnt(0)
	s_add_u32 s0, s44, s2
	v_addc_co_u32_e32 v9, vcc, 0, v31, vcc
	s_movk_i32 s16, 0x6000
	s_addc_u32 s1, s45, 0
	v_add_co_u32_e32 v10, vcc, s16, v30
	v_lshlrev_b32_e32 v38, 4, v156
	s_add_u32 s2, s46, s2
	v_addc_co_u32_e32 v11, vcc, 0, v31, vcc
	s_mov_b32 s15, 0x8000
	s_addc_u32 s3, s47, 0
	global_load_dwordx4 v[0:3], v38, s[0:1]
	global_load_dwordx4 v[4:7], v38, s[2:3]
	global_load_dwordx2 v[42:43], v[8:9], off offset:-4096
	global_load_dwordx2 v[32:33], v[8:9], off
	global_load_dwordx2 v[28:29], v[10:11], off offset:-4096
	global_load_dwordx2 v[26:27], v[10:11], off
	v_add_co_u32_e32 v8, vcc, s15, v30
	s_mov_b32 s14, 0xa000
	s_nop 0
	v_addc_co_u32_e32 v9, vcc, 0, v31, vcc
	v_add_co_u32_e32 v10, vcc, s14, v30
	s_mov_b32 s13, 0xc000
	s_nop 0
	v_addc_co_u32_e32 v11, vcc, 0, v31, vcc
	global_load_dwordx2 v[24:25], v[8:9], off offset:-4096
	global_load_dwordx2 v[22:23], v[8:9], off
	global_load_dwordx2 v[20:21], v[10:11], off offset:-4096
	global_load_dwordx2 v[18:19], v[10:11], off
	v_add_co_u32_e32 v8, vcc, s13, v30
	s_mov_b32 s12, 0xe000
	s_nop 0
	v_addc_co_u32_e32 v9, vcc, 0, v31, vcc
	v_add_co_u32_e32 v36, vcc, s12, v30
	s_mov_b32 s0, 0xf000
	s_nop 0
	v_addc_co_u32_e32 v37, vcc, 0, v31, vcc
	global_load_dwordx2 v[16:17], v[8:9], off offset:-4096
	global_load_dwordx2 v[14:15], v[8:9], off
	global_load_dwordx2 v[12:13], v[36:37], off offset:-4096
	global_load_dwordx2 v[10:11], v[36:37], off
	v_add_co_u32_e32 v36, vcc, s0, v30
	v_lshl_add_u32 v107, v137, 15, 0
	s_nop 0
	v_addc_co_u32_e32 v37, vcc, 0, v31, vcc
	v_lshlrev_b32_e32 v108, 2, v138
	global_load_dwordx2 v[96:97], v[30:31], off
	global_load_dwordx2 v[70:71], v[34:35], off offset:-4096
	global_load_dwordx2 v[68:69], v[34:35], off
	global_load_dwordx2 v[8:9], v[36:37], off
	s_nop 15
	s_nop 15
	s_nop 7
	v_accvgpr_read_b32 v30, a0
	v_accvgpr_read_b32 v31, a1
	v_accvgpr_read_b32 v34, a2
	v_accvgpr_read_b32 v35, a3
	v_accvgpr_read_b32 v36, a4
	v_accvgpr_read_b32 v37, a5
	v_accvgpr_read_b32 v39, a6
	v_accvgpr_read_b32 v40, a7
	v_accvgpr_read_b32 v41, a8
	v_accvgpr_read_b32 v44, a9
	v_accvgpr_read_b32 v45, a10
	v_accvgpr_read_b32 v46, a11
	v_accvgpr_read_b32 v47, a12
	v_accvgpr_read_b32 v48, a13
	v_accvgpr_read_b32 v49, a14
	v_accvgpr_read_b32 v50, a15
	v_add3_u32 v107, v107, v139, v108
	v_accvgpr_read_b32 v51, a16
	v_accvgpr_read_b32 v52, a17
	v_accvgpr_read_b32 v53, a18
	v_accvgpr_read_b32 v54, a19
	v_accvgpr_read_b32 v55, a20
	v_accvgpr_read_b32 v56, a21
	v_accvgpr_read_b32 v57, a22
	v_accvgpr_read_b32 v58, a23
	v_accvgpr_read_b32 v59, a24
	v_accvgpr_read_b32 v62, a25
	v_accvgpr_read_b32 v63, a26
	v_accvgpr_read_b32 v64, a27
	v_accvgpr_read_b32 v65, a28
	v_accvgpr_read_b32 v66, a29
	v_accvgpr_read_b32 v67, a30
	v_accvgpr_read_b32 v72, a31
	s_mov_b32 s28, 0x3727c5ac
	v_accvgpr_read_b32 v73, a32
	v_accvgpr_read_b32 v74, a33
	v_accvgpr_read_b32 v75, a34
	v_accvgpr_read_b32 v76, a35
	v_accvgpr_read_b32 v77, a36
	v_accvgpr_read_b32 v78, a37
	v_accvgpr_read_b32 v79, a38
	v_accvgpr_read_b32 v80, a39
	v_accvgpr_read_b32 v81, a40
	v_accvgpr_read_b32 v82, a41
	v_accvgpr_read_b32 v83, a42
	v_accvgpr_read_b32 v84, a43
	v_accvgpr_read_b32 v85, a44
	v_accvgpr_read_b32 v86, a45
	v_accvgpr_read_b32 v87, a46
	v_accvgpr_read_b32 v88, a47
	v_lshl_add_u64 v[60:61], s[48:49], 0, v[60:61]
	v_accvgpr_read_b32 v89, a48
	v_accvgpr_read_b32 v90, a49
	v_accvgpr_read_b32 v91, a50
	v_accvgpr_read_b32 v92, a51
	v_accvgpr_read_b32 v93, a52
	v_accvgpr_read_b32 v94, a53
	v_accvgpr_read_b32 v95, a54
	v_accvgpr_read_b32 v98, a55
	v_accvgpr_read_b32 v99, a56
	v_accvgpr_read_b32 v100, a57
	v_accvgpr_read_b32 v101, a58
	v_accvgpr_read_b32 v102, a59
	v_accvgpr_read_b32 v103, a60
	v_accvgpr_read_b32 v104, a61
	v_accvgpr_read_b32 v105, a62
	v_accvgpr_read_b32 v106, a63
	s_nop 0
	v_accvgpr_read_b32 v108, a64
	v_accvgpr_read_b32 v109, a65
	v_accvgpr_read_b32 v110, a66
	v_accvgpr_read_b32 v111, a67
	v_accvgpr_read_b32 v112, a68
	v_accvgpr_read_b32 v113, a69
	v_accvgpr_read_b32 v114, a70
	v_accvgpr_read_b32 v115, a71
	v_accvgpr_read_b32 v116, a72
	v_accvgpr_read_b32 v117, a73
	v_accvgpr_read_b32 v118, a74
	v_accvgpr_read_b32 v119, a75
	v_accvgpr_read_b32 v120, a76
	v_accvgpr_read_b32 v121, a77
	v_accvgpr_read_b32 v122, a78
	v_accvgpr_read_b32 v123, a79
	s_nop 0
	v_accvgpr_read_b32 v124, a80
	v_accvgpr_read_b32 v125, a81
	v_accvgpr_read_b32 v126, a82
	v_accvgpr_read_b32 v127, a83
	v_accvgpr_read_b32 v128, a84
	v_accvgpr_read_b32 v129, a85
	v_accvgpr_read_b32 v130, a86
	v_accvgpr_read_b32 v131, a87
	v_accvgpr_read_b32 v132, a88
	v_accvgpr_read_b32 v133, a89
	v_accvgpr_read_b32 v134, a90
	v_accvgpr_read_b32 v135, a91
	v_accvgpr_read_b32 v137, a92
	v_accvgpr_read_b32 v138, a93
	v_accvgpr_read_b32 v139, a94
	v_accvgpr_read_b32 v140, a95
	s_nop 0
	v_accvgpr_read_b32 v141, a96
	v_accvgpr_read_b32 v142, a97
	v_accvgpr_read_b32 v144, a98
	v_accvgpr_read_b32 v145, a99
	v_accvgpr_read_b32 v146, a100
	v_accvgpr_read_b32 v147, a101
	v_accvgpr_read_b32 v148, a102
	v_accvgpr_read_b32 v149, a103
	v_accvgpr_read_b32 v150, a104
	v_accvgpr_read_b32 v151, a105
	v_accvgpr_read_b32 v152, a106
	v_accvgpr_read_b32 v153, a107
	v_accvgpr_read_b32 v154, a108
	v_accvgpr_read_b32 v155, a109
	v_accvgpr_read_b32 v156, a110
	v_accvgpr_read_b32 v157, a111
	s_nop 0
	v_accvgpr_read_b32 v158, a112
	v_accvgpr_read_b32 v159, a113
	v_accvgpr_read_b32 v160, a114
	v_accvgpr_read_b32 v161, a115
	v_accvgpr_read_b32 v162, a116
	v_accvgpr_read_b32 v163, a117
	v_accvgpr_read_b32 v164, a118
	v_accvgpr_read_b32 v165, a119
	v_accvgpr_read_b32 v166, a120
	v_accvgpr_read_b32 v167, a121
	v_accvgpr_read_b32 v168, a122
	v_accvgpr_read_b32 v169, a123
	v_accvgpr_read_b32 v170, a124
	v_accvgpr_read_b32 v171, a125
	v_accvgpr_read_b32 v172, a126
	v_accvgpr_read_b32 v173, a127
	s_waitcnt vmcnt(0)
	s_barrier
	ds_write2_b32 v107, v30, v51 offset1:32
	v_add_u32_e32 v30, 0x400, v107
	ds_write2_b32 v30, v31, v52 offset1:32
	v_add_u32_e32 v31, 0x800, v107
	ds_write2_b32 v31, v34, v53 offset1:32
	v_add_u32_e32 v34, 0xc00, v107
	ds_write2_b32 v34, v35, v54 offset1:32
	v_add_u32_e32 v35, 0x2000, v107
	ds_write2_b32 v35, v36, v55 offset1:32
	v_add_u32_e32 v36, 0x2400, v107
	ds_write2_b32 v36, v37, v56 offset1:32
	v_add_u32_e32 v37, 0x2800, v107
	ds_write2_b32 v37, v39, v57 offset1:32
	v_add_u32_e32 v39, 0x2c00, v107
	ds_write2_b32 v39, v40, v58 offset1:32
	v_add_u32_e32 v40, 0x4000, v107
	ds_write2_b32 v40, v41, v59 offset1:32
	v_add_u32_e32 v41, 0x4400, v107
	ds_write2_b32 v41, v44, v62 offset1:32
	v_add_u32_e32 v44, 0x4800, v107
	ds_write2_b32 v44, v45, v63 offset1:32
	v_add_u32_e32 v45, 0x4c00, v107
	ds_write2_b32 v45, v46, v64 offset1:32
	v_add_u32_e32 v46, 0x6000, v107
	ds_write2_b32 v46, v47, v65 offset1:32
	v_add_u32_e32 v47, 0x6400, v107
	ds_write2_b32 v47, v48, v66 offset1:32
	v_add_u32_e32 v48, 0x6800, v107
	ds_write2_b32 v48, v49, v67 offset1:32
	v_add_u32_e32 v49, 0x6c00, v107
	ds_write2_b32 v49, v50, v72 offset1:32
	ds_write2_b32 v107, v73, v89 offset0:64 offset1:96
	ds_write2_b32 v30, v74, v90 offset0:64 offset1:96
	ds_write2_b32 v31, v75, v91 offset0:64 offset1:96
	ds_write2_b32 v34, v76, v92 offset0:64 offset1:96
	ds_write2_b32 v35, v77, v93 offset0:64 offset1:96
	ds_write2_b32 v36, v78, v94 offset0:64 offset1:96
	ds_write2_b32 v37, v79, v95 offset0:64 offset1:96
	ds_write2_b32 v39, v80, v98 offset0:64 offset1:96
	ds_write2_b32 v40, v81, v99 offset0:64 offset1:96
	ds_write2_b32 v41, v82, v100 offset0:64 offset1:96
	ds_write2_b32 v44, v83, v101 offset0:64 offset1:96
	ds_write2_b32 v45, v84, v102 offset0:64 offset1:96
	ds_write2_b32 v46, v85, v103 offset0:64 offset1:96
	ds_write2_b32 v47, v86, v104 offset0:64 offset1:96
	ds_write2_b32 v48, v87, v105 offset0:64 offset1:96
	ds_write2_b32 v49, v88, v106 offset0:64 offset1:96
	ds_write2_b32 v107, v108, v124 offset0:128 offset1:160
	ds_write2_b32 v30, v109, v125 offset0:128 offset1:160
	ds_write2_b32 v31, v110, v126 offset0:128 offset1:160
	ds_write2_b32 v34, v111, v127 offset0:128 offset1:160
	ds_write2_b32 v35, v112, v128 offset0:128 offset1:160
	ds_write2_b32 v36, v113, v129 offset0:128 offset1:160
	ds_write2_b32 v37, v114, v130 offset0:128 offset1:160
	ds_write2_b32 v39, v115, v131 offset0:128 offset1:160
	ds_write2_b32 v40, v116, v132 offset0:128 offset1:160
	ds_write2_b32 v41, v117, v133 offset0:128 offset1:160
	ds_write2_b32 v44, v118, v134 offset0:128 offset1:160
	ds_write2_b32 v45, v119, v135 offset0:128 offset1:160
	ds_write2_b32 v46, v120, v137 offset0:128 offset1:160
	ds_write2_b32 v47, v121, v138 offset0:128 offset1:160
	ds_write2_b32 v48, v122, v139 offset0:128 offset1:160
	ds_write2_b32 v49, v123, v140 offset0:128 offset1:160
	ds_write2_b32 v107, v141, v158 offset0:192 offset1:224
	ds_write2_b32 v30, v142, v159 offset0:192 offset1:224
	ds_write2_b32 v31, v144, v160 offset0:192 offset1:224
	ds_write2_b32 v34, v145, v161 offset0:192 offset1:224
	ds_write2_b32 v35, v146, v162 offset0:192 offset1:224
	ds_write2_b32 v36, v147, v163 offset0:192 offset1:224
	ds_write2_b32 v37, v148, v164 offset0:192 offset1:224
	ds_write2_b32 v39, v149, v165 offset0:192 offset1:224
	ds_write2_b32 v40, v150, v166 offset0:192 offset1:224
	ds_write2_b32 v41, v151, v167 offset0:192 offset1:224
	ds_write2_b32 v44, v152, v168 offset0:192 offset1:224
	ds_write2_b32 v45, v153, v169 offset0:192 offset1:224
	ds_write2_b32 v46, v154, v170 offset0:192 offset1:224
	ds_write2_b32 v47, v155, v171 offset0:192 offset1:224
	ds_write2_b32 v48, v156, v172 offset0:192 offset1:224
	ds_write2_b32 v49, v157, v173 offset0:192 offset1:224
	v_lshl_add_u32 v30, v136, 15, 0
	v_add3_u32 v116, v30, v143, v38
	v_add_u32_e32 v30, 0x10000, v116
	s_waitcnt lgkmcnt(0)
	s_barrier
	ds_read_b128 v[34:37], v30
	ds_read_b128 v[38:41], v116
	ds_read_b128 v[44:47], v116 offset:1024
	v_add_u32_e32 v30, 0x10400, v116
	ds_read_b128 v[48:51], v30
	s_waitcnt lgkmcnt(2)
	v_pk_add_f32 v[102:103], v[40:41], v[36:37]
	v_pk_add_f32 v[104:105], v[38:39], v[34:35]
	v_add_u32_e32 v38, 0x10800, v116
	v_mov_b32_e32 v34, v104
	v_mov_b32_e32 v35, v103
	ds_read_b128 v[38:41], v38
	v_pk_mov_b32 v[30:31], v[104:105], v[102:103] op_sel:[1,0]
	s_waitcnt lgkmcnt(1)
	v_pk_add_f32 v[98:99], v[46:47], v[50:51]
	v_pk_add_f32 v[132:133], v[30:31], v[34:35]
	v_pk_add_f32 v[100:101], v[44:45], v[48:49]
	ds_read_b128 v[34:37], v116 offset:2048
	v_pk_mov_b32 v[30:31], v[100:101], v[98:99] op_sel:[1,0]
	v_mov_b32_e32 v44, v100
	v_mov_b32_e32 v45, v99
	v_pk_add_f32 v[122:123], v[30:31], v[44:45]
	v_add_u32_e32 v30, 0x10c00, v116
	ds_read_b128 v[44:47], v116 offset:3072
	ds_read_b128 v[48:51], v30
	s_waitcnt lgkmcnt(2)
	v_pk_add_f32 v[92:93], v[36:37], v[40:41]
	v_pk_add_f32 v[94:95], v[34:35], v[38:39]
	v_mov_b32_e32 v35, v93
	v_pk_mov_b32 v[30:31], v[94:95], v[92:93] op_sel:[1,0]
	v_mov_b32_e32 v34, v94
	v_pk_add_f32 v[118:119], v[30:31], v[34:35]
	v_add_u32_e32 v34, 0x11000, v116
	s_waitcnt lgkmcnt(0)
	v_pk_add_f32 v[88:89], v[46:47], v[50:51]
	v_pk_add_f32 v[90:91], v[44:45], v[48:49]
	ds_read_b128 v[34:37], v34
	ds_read_b128 v[38:41], v116 offset:4096
	ds_read_b128 v[44:47], v116 offset:5120
	v_pk_mov_b32 v[30:31], v[90:91], v[88:89] op_sel:[1,0]
	v_mov_b32_e32 v52, v90
	v_add_u32_e32 v48, 0x11400, v116
	v_mov_b32_e32 v53, v89
	ds_read_b128 v[48:51], v48
	v_pk_add_f32 v[120:121], v[30:31], v[52:53]
	v_add_u32_e32 v30, 0x11800, v116
	s_waitcnt lgkmcnt(2)
	v_pk_add_f32 v[84:85], v[40:41], v[36:37]
	v_pk_add_f32 v[86:87], v[38:39], v[34:35]
	ds_read_b128 v[34:37], v116 offset:6144
	ds_read_b128 v[38:41], v30
	v_add_u32_e32 v30, 0x11c00, v116
	s_waitcnt lgkmcnt(2)
	v_pk_add_f32 v[80:81], v[46:47], v[50:51]
	v_pk_add_f32 v[82:83], v[44:45], v[48:49]
	ds_read_b128 v[48:51], v30
	v_add_u32_e32 v30, 0x12000, v116
	ds_read_b128 v[44:47], v116 offset:7168
	s_waitcnt lgkmcnt(2)
	v_pk_add_f32 v[74:75], v[36:37], v[40:41]
	v_pk_add_f32 v[76:77], v[34:35], v[38:39]
	ds_read_b128 v[34:37], v30
	ds_read_b128 v[38:41], v116 offset:8192
	ds_read_b128 v[52:55], v116 offset:9216
	v_add_u32_e32 v30, 0x12400, v116
	ds_read_b128 v[56:59], v30
	s_waitcnt lgkmcnt(4)
	v_pk_add_f32 v[72:73], v[46:47], v[50:51]
	s_waitcnt lgkmcnt(2)
	v_pk_add_f32 v[64:65], v[40:41], v[36:37]
	v_pk_add_f32 v[66:67], v[38:39], v[34:35]
	ds_read_b128 v[34:37], v116 offset:10240
	v_add_u32_e32 v30, 0x12800, v116
	ds_read_b128 v[38:41], v30
	v_pk_add_f32 v[78:79], v[44:45], v[48:49]
	ds_read_b128 v[44:47], v116 offset:11264
	v_add_u32_e32 v30, 0x12c00, v116
	ds_read_b128 v[48:51], v30
	v_add_u32_e32 v30, 0x13000, v116
	s_waitcnt lgkmcnt(4)
	v_pk_add_f32 v[58:59], v[54:55], v[58:59]
	v_pk_add_f32 v[62:63], v[52:53], v[56:57]
	s_waitcnt lgkmcnt(2)
	v_pk_add_f32 v[52:53], v[36:37], v[40:41]
	v_pk_add_f32 v[54:55], v[34:35], v[38:39]
	ds_read_b128 v[34:37], v30
	ds_read_b128 v[38:41], v116 offset:12288
	ds_read_b128 v[106:109], v116 offset:13312
	v_add_u32_e32 v30, 0x13400, v116
	ds_read_b128 v[110:113], v30
	s_waitcnt lgkmcnt(4)
	v_pk_add_f32 v[50:51], v[46:47], v[50:51]
	v_pk_add_f32 v[56:57], v[44:45], v[48:49]
	s_waitcnt lgkmcnt(2)
	v_pk_add_f32 v[46:47], v[40:41], v[36:37]
	v_pk_add_f32 v[48:49], v[38:39], v[34:35]
	ds_read_b128 v[34:37], v116 offset:14336
	v_add_u32_e32 v30, 0x13800, v116
	s_waitcnt lgkmcnt(1)
	v_pk_add_f32 v[40:41], v[108:109], v[112:113]
	ds_read_b128 v[112:115], v30
	v_pk_add_f32 v[44:45], v[106:107], v[110:111]
	ds_read_b128 v[106:109], v116 offset:15360
	v_add_u32_e32 v30, 0x13c00, v116
	ds_read_b128 v[124:127], v30
	s_waitcnt lgkmcnt(2)
	v_pk_add_f32 v[38:39], v[34:35], v[112:113]
	v_pk_mov_b32 v[30:31], v[86:87], v[84:85] op_sel:[1,0]
	v_mov_b32_e32 v34, v86
	v_mov_b32_e32 v35, v85
	v_pk_add_f32 v[136:137], v[30:31], v[34:35]
	v_pk_mov_b32 v[30:31], v[82:83], v[80:81] op_sel:[1,0]
	v_mov_b32_e32 v34, v82
	v_mov_b32_e32 v35, v81
	v_pk_add_f32 v[134:135], v[30:31], v[34:35]
	s_waitcnt lgkmcnt(0)
	v_pk_add_f32 v[30:31], v[108:109], v[126:127]
	v_pk_add_f32 v[34:35], v[106:107], v[124:125]
	v_pk_mov_b32 v[106:107], v[76:77], v[74:75] op_sel:[1,0]
	v_mov_b32_e32 v108, v76
	v_mov_b32_e32 v109, v75
	v_add_f32_e32 v132, v132, v133
	v_pk_add_f32 v[130:131], v[106:107], v[108:109]
	v_pk_mov_b32 v[106:107], v[78:79], v[72:73] op_sel:[1,0]
	v_mov_b32_e32 v108, v78
	v_mov_b32_e32 v109, v73
	v_add_f32_dpp v132, v132, v132 quad_perm:[1,0,3,2] row_mask:0xf bank_mask:0xf bound_ctrl:1
	v_pk_add_f32 v[128:129], v[106:107], v[108:109]
	v_mov_b32_e32 v106, v66
	v_mov_b32_e32 v107, v65
	v_pk_mov_b32 v[108:109], v[66:67], v[64:65] op_sel:[1,0]
	v_add_f32_dpp v132, v132, v132 quad_perm:[2,3,0,1] row_mask:0xf bank_mask:0xf bound_ctrl:1
	v_add_f32_e32 v122, v122, v123
	v_pk_add_f32 v[126:127], v[108:109], v[106:107]
	v_mov_b32_e32 v106, v62
	v_mov_b32_e32 v107, v59
	v_pk_mov_b32 v[108:109], v[62:63], v[58:59] op_sel:[1,0]
	v_add_f32_dpp v132, v132, v132 row_half_mirror row_mask:0xf bank_mask:0xf bound_ctrl:1
	v_add_f32_dpp v122, v122, v122 quad_perm:[1,0,3,2] row_mask:0xf bank_mask:0xf bound_ctrl:1
	v_pk_add_f32 v[124:125], v[108:109], v[106:107]
	v_mov_b32_e32 v106, v54
	v_mov_b32_e32 v107, v53
	v_pk_mov_b32 v[108:109], v[54:55], v[52:53] op_sel:[1,0]
	v_add_f32_dpp v132, v132, v132 row_mirror row_mask:0xf bank_mask:0xf bound_ctrl:1
	v_add_f32_dpp v122, v122, v122 quad_perm:[2,3,0,1] row_mask:0xf bank_mask:0xf bound_ctrl:1
	v_add_f32_e32 v118, v118, v119
	v_pk_add_f32 v[116:117], v[108:109], v[106:107]
	v_mov_b32_e32 v106, v56
	v_mov_b32_e32 v107, v51
	v_pk_mov_b32 v[108:109], v[56:57], v[50:51] op_sel:[1,0]
	v_readlane_b32 s2, v132, 16
	v_readlane_b32 s3, v132, 48
	v_add_f32_dpp v122, v122, v122 row_half_mirror row_mask:0xf bank_mask:0xf bound_ctrl:1
	v_add_f32_dpp v118, v118, v118 quad_perm:[1,0,3,2] row_mask:0xf bank_mask:0xf bound_ctrl:1
	v_pk_add_f32 v[36:37], v[36:37], v[114:115]
	v_pk_add_f32 v[114:115], v[108:109], v[106:107]
	v_mov_b32_e32 v106, v48
	v_mov_b32_e32 v107, v47
	v_pk_mov_b32 v[108:109], v[48:49], v[46:47] op_sel:[1,0]
	v_readlane_b32 s0, v132, 0
	v_readlane_b32 s1, v132, 32
	v_mov_b32_e32 v132, s2
	v_mov_b32_e32 v133, s3
	v_add_f32_dpp v122, v122, v122 row_mirror row_mask:0xf bank_mask:0xf bound_ctrl:1
	v_add_f32_dpp v118, v118, v118 quad_perm:[2,3,0,1] row_mask:0xf bank_mask:0xf bound_ctrl:1
	v_add_f32_e32 v120, v120, v121
	v_pk_add_f32 v[112:113], v[108:109], v[106:107]
	v_mov_b32_e32 v106, v44
	v_mov_b32_e32 v107, v41
	v_pk_mov_b32 v[108:109], v[44:45], v[40:41] op_sel:[1,0]
	v_pk_add_f32 v[132:133], s[0:1], v[132:133]
	v_readlane_b32 s2, v122, 16
	v_readlane_b32 s3, v122, 48
	v_add_f32_dpp v118, v118, v118 row_half_mirror row_mask:0xf bank_mask:0xf bound_ctrl:1
	v_add_f32_dpp v120, v120, v120 quad_perm:[1,0,3,2] row_mask:0xf bank_mask:0xf bound_ctrl:1
	v_pk_add_f32 v[110:111], v[108:109], v[106:107]
	v_mov_b32_e32 v106, v38
	v_mov_b32_e32 v107, v37
	v_pk_mov_b32 v[108:109], v[38:39], v[36:37] op_sel:[1,0]
	v_add_f32_e32 v132, v132, v133
	v_readlane_b32 s0, v122, 0
	v_readlane_b32 s1, v122, 32
	v_mov_b32_e32 v122, s2
	v_mov_b32_e32 v123, s3
	v_add_f32_dpp v118, v118, v118 row_mirror row_mask:0xf bank_mask:0xf bound_ctrl:1
	v_add_f32_dpp v120, v120, v120 quad_perm:[2,3,0,1] row_mask:0xf bank_mask:0xf bound_ctrl:1
	v_add_f32_e32 v136, v136, v137
	v_pk_add_f32 v[108:109], v[108:109], v[106:107]
	v_mov_b32_e32 v106, v34
	v_mov_b32_e32 v107, v31
	v_pk_mov_b32 v[138:139], v[34:35], v[30:31] op_sel:[1,0]
	v_fmamk_f32 v105, v132, 0xbb800000, v105
	v_fmac_f32_e32 v104, 0xbb800000, v132
	v_fmamk_f32 v103, v132, 0xbb800000, v103
	v_fmac_f32_e32 v102, 0xbb800000, v132
	v_pk_add_f32 v[122:123], s[0:1], v[122:123]
	v_readlane_b32 s2, v118, 16
	v_readlane_b32 s3, v118, 48
	v_add_f32_dpp v120, v120, v120 row_half_mirror row_mask:0xf bank_mask:0xf bound_ctrl:1
	v_add_f32_dpp v136, v136, v136 quad_perm:[1,0,3,2] row_mask:0xf bank_mask:0xf bound_ctrl:1
	v_pk_add_f32 v[106:107], v[138:139], v[106:107]
	v_pk_mul_f32 v[132:133], v[102:103], v[102:103]
	v_pk_mul_f32 v[138:139], v[104:105], v[104:105]
	v_add_f32_e32 v122, v122, v123
	v_readlane_b32 s0, v118, 0
	v_readlane_b32 s1, v118, 32
	v_mov_b32_e32 v118, s2
	v_mov_b32_e32 v119, s3
	v_add_f32_dpp v120, v120, v120 row_mirror row_mask:0xf bank_mask:0xf bound_ctrl:1
	v_add_f32_dpp v136, v136, v136 quad_perm:[2,3,0,1] row_mask:0xf bank_mask:0xf bound_ctrl:1
	v_add_f32_e32 v134, v134, v135
	v_pk_mov_b32 v[140:141], v[138:139], v[132:133] op_sel:[1,0]
	v_mov_b32_e32 v139, v133
	v_fmamk_f32 v101, v122, 0xbb800000, v101
	v_fmac_f32_e32 v100, 0xbb800000, v122
	v_fmamk_f32 v99, v122, 0xbb800000, v99
	v_fmac_f32_e32 v98, 0xbb800000, v122
	v_pk_add_f32 v[118:119], s[0:1], v[118:119]
	v_readlane_b32 s2, v120, 16
	v_readlane_b32 s3, v120, 48
	v_add_f32_dpp v136, v136, v136 row_half_mirror row_mask:0xf bank_mask:0xf bound_ctrl:1
	v_add_f32_dpp v134, v134, v134 quad_perm:[1,0,3,2] row_mask:0xf bank_mask:0xf bound_ctrl:1
	v_pk_add_f32 v[132:133], v[140:141], v[138:139]
	v_pk_mul_f32 v[122:123], v[98:99], v[98:99]
	v_pk_mul_f32 v[138:139], v[100:101], v[100:101]
	v_add_f32_e32 v118, v118, v119
	v_readlane_b32 s0, v120, 0
	v_readlane_b32 s1, v120, 32
	v_mov_b32_e32 v120, s2
	v_mov_b32_e32 v121, s3
	v_add_f32_dpp v136, v136, v136 row_mirror row_mask:0xf bank_mask:0xf bound_ctrl:1
	v_add_f32_dpp v134, v134, v134 quad_perm:[2,3,0,1] row_mask:0xf bank_mask:0xf bound_ctrl:1
	v_add_f32_e32 v130, v130, v131
	v_pk_mov_b32 v[140:141], v[138:139], v[122:123] op_sel:[1,0]
	v_mov_b32_e32 v139, v123
	v_fmamk_f32 v95, v118, 0xbb800000, v95
	v_fmac_f32_e32 v94, 0xbb800000, v118
	v_fmamk_f32 v93, v118, 0xbb800000, v93
	v_fmac_f32_e32 v92, 0xbb800000, v118
	v_pk_add_f32 v[120:121], s[0:1], v[120:121]
	v_readlane_b32 s2, v136, 16
	v_readlane_b32 s3, v136, 48
	v_add_f32_dpp v134, v134, v134 row_half_mirror row_mask:0xf bank_mask:0xf bound_ctrl:1
	v_add_f32_dpp v130, v130, v130 quad_perm:[1,0,3,2] row_mask:0xf bank_mask:0xf bound_ctrl:1
	v_pk_add_f32 v[122:123], v[140:141], v[138:139]
	v_pk_mul_f32 v[118:119], v[92:93], v[92:93]
	v_pk_mul_f32 v[138:139], v[94:95], v[94:95]
	v_add_f32_e32 v120, v120, v121
	v_readlane_b32 s0, v136, 0
	v_readlane_b32 s1, v136, 32
	v_mov_b32_e32 v136, s2
	v_mov_b32_e32 v137, s3
	v_add_f32_dpp v134, v134, v134 row_mirror row_mask:0xf bank_mask:0xf bound_ctrl:1
	v_add_f32_dpp v130, v130, v130 quad_perm:[2,3,0,1] row_mask:0xf bank_mask:0xf bound_ctrl:1
	v_add_f32_e32 v128, v128, v129
	v_pk_mov_b32 v[140:141], v[138:139], v[118:119] op_sel:[1,0]
	v_mov_b32_e32 v139, v119
	v_fmamk_f32 v91, v120, 0xbb800000, v91
	v_fmac_f32_e32 v90, 0xbb800000, v120
	v_fmamk_f32 v89, v120, 0xbb800000, v89
	v_fmac_f32_e32 v88, 0xbb800000, v120
	v_pk_add_f32 v[136:137], s[0:1], v[136:137]
	v_readlane_b32 s2, v134, 16
	v_readlane_b32 s3, v134, 48
	v_add_f32_dpp v130, v130, v130 row_half_mirror row_mask:0xf bank_mask:0xf bound_ctrl:1
	v_add_f32_dpp v128, v128, v128 quad_perm:[1,0,3,2] row_mask:0xf bank_mask:0xf bound_ctrl:1
	v_pk_add_f32 v[118:119], v[140:141], v[138:139]
	v_pk_mul_f32 v[120:121], v[88:89], v[88:89]
	v_pk_mul_f32 v[138:139], v[90:91], v[90:91]
	v_add_f32_e32 v136, v136, v137
	v_readlane_b32 s0, v134, 0
	v_readlane_b32 s1, v134, 32
	v_mov_b32_e32 v134, s2
	v_mov_b32_e32 v135, s3
	v_add_f32_dpp v130, v130, v130 row_mirror row_mask:0xf bank_mask:0xf bound_ctrl:1
	v_add_f32_dpp v128, v128, v128 quad_perm:[2,3,0,1] row_mask:0xf bank_mask:0xf bound_ctrl:1
	v_add_f32_e32 v126, v126, v127
	v_pk_mov_b32 v[140:141], v[138:139], v[120:121] op_sel:[1,0]
	v_mov_b32_e32 v139, v121
	v_fmamk_f32 v87, v136, 0xbb800000, v87
	v_fmac_f32_e32 v86, 0xbb800000, v136
	v_fmamk_f32 v85, v136, 0xbb800000, v85
	v_fmac_f32_e32 v84, 0xbb800000, v136
	v_pk_add_f32 v[134:135], s[0:1], v[134:135]
	v_readlane_b32 s2, v130, 16
	v_readlane_b32 s3, v130, 48
	v_add_f32_dpp v128, v128, v128 row_half_mirror row_mask:0xf bank_mask:0xf bound_ctrl:1
	v_add_f32_dpp v126, v126, v126 quad_perm:[1,0,3,2] row_mask:0xf bank_mask:0xf bound_ctrl:1
	v_pk_add_f32 v[120:121], v[140:141], v[138:139]
	v_pk_mul_f32 v[136:137], v[84:85], v[84:85]
	v_pk_mul_f32 v[138:139], v[86:87], v[86:87]
	v_add_f32_e32 v134, v134, v135
	v_readlane_b32 s0, v130, 0
	v_readlane_b32 s1, v130, 32
	v_mov_b32_e32 v130, s2
	v_mov_b32_e32 v131, s3
	v_add_f32_dpp v128, v128, v128 row_mirror row_mask:0xf bank_mask:0xf bound_ctrl:1
	v_add_f32_dpp v126, v126, v126 quad_perm:[2,3,0,1] row_mask:0xf bank_mask:0xf bound_ctrl:1
	v_add_f32_e32 v124, v124, v125
	v_pk_mov_b32 v[140:141], v[138:139], v[136:137] op_sel:[1,0]
	v_mov_b32_e32 v139, v137
	v_fmamk_f32 v83, v134, 0xbb800000, v83
	v_fmac_f32_e32 v82, 0xbb800000, v134
	v_fmamk_f32 v81, v134, 0xbb800000, v81
	v_fmac_f32_e32 v80, 0xbb800000, v134
	v_pk_add_f32 v[130:131], s[0:1], v[130:131]
	v_readlane_b32 s2, v128, 16
	v_readlane_b32 s3, v128, 48
	v_add_f32_dpp v126, v126, v126 row_half_mirror row_mask:0xf bank_mask:0xf bound_ctrl:1
	v_add_f32_dpp v124, v124, v124 quad_perm:[1,0,3,2] row_mask:0xf bank_mask:0xf bound_ctrl:1
	v_pk_add_f32 v[136:137], v[140:141], v[138:139]
	v_pk_mul_f32 v[134:135], v[80:81], v[80:81]
	v_pk_mul_f32 v[138:139], v[82:83], v[82:83]
	v_add_f32_e32 v130, v130, v131
	v_readlane_b32 s0, v128, 0
	v_readlane_b32 s1, v128, 32
	v_mov_b32_e32 v128, s2
	v_mov_b32_e32 v129, s3
	v_add_f32_dpp v126, v126, v126 row_mirror row_mask:0xf bank_mask:0xf bound_ctrl:1
	v_add_f32_dpp v124, v124, v124 quad_perm:[2,3,0,1] row_mask:0xf bank_mask:0xf bound_ctrl:1
	v_add_f32_e32 v116, v116, v117
	v_pk_mov_b32 v[140:141], v[138:139], v[134:135] op_sel:[1,0]
	v_mov_b32_e32 v139, v135
	v_fmamk_f32 v77, v130, 0xbb800000, v77
	v_fmac_f32_e32 v76, 0xbb800000, v130
	v_fmamk_f32 v75, v130, 0xbb800000, v75
	v_fmac_f32_e32 v74, 0xbb800000, v130
	v_pk_add_f32 v[128:129], s[0:1], v[128:129]
	v_readlane_b32 s2, v126, 16
	v_readlane_b32 s3, v126, 48
	v_add_f32_dpp v124, v124, v124 row_half_mirror row_mask:0xf bank_mask:0xf bound_ctrl:1
	v_add_f32_dpp v116, v116, v116 quad_perm:[1,0,3,2] row_mask:0xf bank_mask:0xf bound_ctrl:1
	v_pk_add_f32 v[134:135], v[140:141], v[138:139]
	v_pk_mul_f32 v[130:131], v[74:75], v[74:75]
	v_pk_mul_f32 v[138:139], v[76:77], v[76:77]
	v_add_f32_e32 v128, v128, v129
	v_readlane_b32 s0, v126, 0
	v_readlane_b32 s1, v126, 32
	v_mov_b32_e32 v126, s2
	v_mov_b32_e32 v127, s3
	v_add_f32_dpp v124, v124, v124 row_mirror row_mask:0xf bank_mask:0xf bound_ctrl:1
	v_add_f32_dpp v116, v116, v116 quad_perm:[2,3,0,1] row_mask:0xf bank_mask:0xf bound_ctrl:1
	v_add_f32_e32 v114, v114, v115
	v_pk_mov_b32 v[140:141], v[138:139], v[130:131] op_sel:[1,0]
	v_mov_b32_e32 v139, v131
	v_fmamk_f32 v79, v128, 0xbb800000, v79
	v_fmac_f32_e32 v78, 0xbb800000, v128
	v_fmamk_f32 v73, v128, 0xbb800000, v73
	v_fmac_f32_e32 v72, 0xbb800000, v128
	v_pk_add_f32 v[126:127], s[0:1], v[126:127]
	v_readlane_b32 s2, v124, 16
	v_readlane_b32 s3, v124, 48
	v_add_f32_dpp v116, v116, v116 row_half_mirror row_mask:0xf bank_mask:0xf bound_ctrl:1
	v_add_f32_dpp v114, v114, v114 quad_perm:[1,0,3,2] row_mask:0xf bank_mask:0xf bound_ctrl:1
	v_pk_add_f32 v[130:131], v[140:141], v[138:139]
	v_pk_mul_f32 v[128:129], v[72:73], v[72:73]
	v_pk_mul_f32 v[138:139], v[78:79], v[78:79]
	v_add_f32_e32 v126, v126, v127
	v_readlane_b32 s0, v124, 0
	v_readlane_b32 s1, v124, 32
	v_mov_b32_e32 v124, s2
	v_mov_b32_e32 v125, s3
	v_add_f32_dpp v116, v116, v116 row_mirror row_mask:0xf bank_mask:0xf bound_ctrl:1
	v_add_f32_dpp v114, v114, v114 quad_perm:[2,3,0,1] row_mask:0xf bank_mask:0xf bound_ctrl:1
	v_add_f32_e32 v112, v112, v113
	v_pk_mov_b32 v[140:141], v[138:139], v[128:129] op_sel:[1,0]
	v_mov_b32_e32 v139, v129
	v_fmamk_f32 v67, v126, 0xbb800000, v67
	v_fmac_f32_e32 v66, 0xbb800000, v126
	v_fmamk_f32 v65, v126, 0xbb800000, v65
	v_fmac_f32_e32 v64, 0xbb800000, v126
	v_pk_add_f32 v[124:125], s[0:1], v[124:125]
	v_readlane_b32 s2, v116, 16
	v_readlane_b32 s3, v116, 48
	v_add_f32_dpp v114, v114, v114 row_half_mirror row_mask:0xf bank_mask:0xf bound_ctrl:1
	v_add_f32_dpp v112, v112, v112 quad_perm:[1,0,3,2] row_mask:0xf bank_mask:0xf bound_ctrl:1
	v_pk_add_f32 v[128:129], v[140:141], v[138:139]
	v_pk_mul_f32 v[126:127], v[64:65], v[64:65]
	v_pk_mul_f32 v[138:139], v[66:67], v[66:67]
	v_add_f32_e32 v124, v124, v125
	v_readlane_b32 s0, v116, 0
	v_readlane_b32 s1, v116, 32
	v_mov_b32_e32 v116, s2
	v_mov_b32_e32 v117, s3
	v_add_f32_dpp v114, v114, v114 row_mirror row_mask:0xf bank_mask:0xf bound_ctrl:1
	v_add_f32_dpp v112, v112, v112 quad_perm:[2,3,0,1] row_mask:0xf bank_mask:0xf bound_ctrl:1
	v_add_f32_e32 v110, v110, v111
	v_pk_mov_b32 v[140:141], v[138:139], v[126:127] op_sel:[1,0]
	v_mov_b32_e32 v139, v127
	v_fmamk_f32 v63, v124, 0xbb800000, v63
	v_fmac_f32_e32 v62, 0xbb800000, v124
	v_fmamk_f32 v59, v124, 0xbb800000, v59
	v_fmac_f32_e32 v58, 0xbb800000, v124
	v_pk_add_f32 v[116:117], s[0:1], v[116:117]
	v_readlane_b32 s2, v114, 16
	v_readlane_b32 s3, v114, 48
	v_add_f32_dpp v112, v112, v112 row_half_mirror row_mask:0xf bank_mask:0xf bound_ctrl:1
	v_add_f32_dpp v110, v110, v110 quad_perm:[1,0,3,2] row_mask:0xf bank_mask:0xf bound_ctrl:1
	v_pk_add_f32 v[126:127], v[140:141], v[138:139]
	v_pk_mul_f32 v[124:125], v[58:59], v[58:59]
	v_pk_mul_f32 v[138:139], v[62:63], v[62:63]
	v_add_f32_e32 v116, v116, v117
	v_readlane_b32 s0, v114, 0
	v_readlane_b32 s1, v114, 32
	v_mov_b32_e32 v114, s2
	v_mov_b32_e32 v115, s3
	v_add_f32_dpp v112, v112, v112 row_mirror row_mask:0xf bank_mask:0xf bound_ctrl:1
	v_add_f32_dpp v110, v110, v110 quad_perm:[2,3,0,1] row_mask:0xf bank_mask:0xf bound_ctrl:1
	v_add_f32_e32 v108, v108, v109
	v_pk_mov_b32 v[140:141], v[138:139], v[124:125] op_sel:[1,0]
	v_mov_b32_e32 v139, v125
	v_fmamk_f32 v55, v116, 0xbb800000, v55
	v_fmac_f32_e32 v54, 0xbb800000, v116
	v_fmamk_f32 v53, v116, 0xbb800000, v53
	v_fmac_f32_e32 v52, 0xbb800000, v116
	v_pk_add_f32 v[114:115], s[0:1], v[114:115]
	v_readlane_b32 s2, v112, 16
	v_readlane_b32 s3, v112, 48
	v_add_f32_dpp v110, v110, v110 row_half_mirror row_mask:0xf bank_mask:0xf bound_ctrl:1
	v_add_f32_dpp v108, v108, v108 quad_perm:[1,0,3,2] row_mask:0xf bank_mask:0xf bound_ctrl:1
	v_pk_add_f32 v[124:125], v[140:141], v[138:139]
	v_pk_mul_f32 v[116:117], v[52:53], v[52:53]
	v_pk_mul_f32 v[138:139], v[54:55], v[54:55]
	v_add_f32_e32 v114, v114, v115
	v_readlane_b32 s0, v112, 0
	v_readlane_b32 s1, v112, 32
	v_mov_b32_e32 v112, s2
	v_mov_b32_e32 v113, s3
	v_add_f32_dpp v110, v110, v110 row_mirror row_mask:0xf bank_mask:0xf bound_ctrl:1
	v_add_f32_dpp v108, v108, v108 quad_perm:[2,3,0,1] row_mask:0xf bank_mask:0xf bound_ctrl:1
	v_add_f32_e32 v106, v106, v107
	v_pk_mov_b32 v[140:141], v[138:139], v[116:117] op_sel:[1,0]
	v_mov_b32_e32 v139, v117
	v_fmamk_f32 v57, v114, 0xbb800000, v57
	v_fmac_f32_e32 v56, 0xbb800000, v114
	v_fmamk_f32 v51, v114, 0xbb800000, v51
	v_fmac_f32_e32 v50, 0xbb800000, v114
	v_pk_add_f32 v[112:113], s[0:1], v[112:113]
	v_readlane_b32 s2, v110, 16
	v_readlane_b32 s3, v110, 48
	v_add_f32_dpp v108, v108, v108 row_half_mirror row_mask:0xf bank_mask:0xf bound_ctrl:1
	v_add_f32_dpp v106, v106, v106 quad_perm:[1,0,3,2] row_mask:0xf bank_mask:0xf bound_ctrl:1
	v_pk_add_f32 v[116:117], v[140:141], v[138:139]
	v_pk_mul_f32 v[114:115], v[50:51], v[50:51]
	v_pk_mul_f32 v[138:139], v[56:57], v[56:57]
	v_add_f32_e32 v112, v112, v113
	v_readlane_b32 s0, v110, 0
	v_readlane_b32 s1, v110, 32
	v_mov_b32_e32 v110, s2
	v_mov_b32_e32 v111, s3
	v_add_f32_dpp v108, v108, v108 row_mirror row_mask:0xf bank_mask:0xf bound_ctrl:1
	v_add_f32_dpp v106, v106, v106 quad_perm:[2,3,0,1] row_mask:0xf bank_mask:0xf bound_ctrl:1
	v_pk_mov_b32 v[140:141], v[138:139], v[114:115] op_sel:[1,0]
	v_mov_b32_e32 v139, v115
	v_fmamk_f32 v49, v112, 0xbb800000, v49
	v_fmac_f32_e32 v48, 0xbb800000, v112
	v_fmamk_f32 v47, v112, 0xbb800000, v47
	v_fmac_f32_e32 v46, 0xbb800000, v112
	v_pk_add_f32 v[110:111], s[0:1], v[110:111]
	v_readlane_b32 s2, v108, 16
	v_readlane_b32 s3, v108, 48
	v_add_f32_dpp v106, v106, v106 row_half_mirror row_mask:0xf bank_mask:0xf bound_ctrl:1
	v_pk_add_f32 v[114:115], v[140:141], v[138:139]
	v_pk_mul_f32 v[112:113], v[46:47], v[46:47]
	v_pk_mul_f32 v[138:139], v[48:49], v[48:49]
	v_add_f32_e32 v110, v110, v111
	v_readlane_b32 s0, v108, 0
	v_readlane_b32 s1, v108, 32
	v_mov_b32_e32 v108, s2
	v_mov_b32_e32 v109, s3
	v_add_f32_dpp v106, v106, v106 row_mirror row_mask:0xf bank_mask:0xf bound_ctrl:1
	v_pk_mov_b32 v[140:141], v[138:139], v[112:113] op_sel:[1,0]
	v_mov_b32_e32 v139, v113
	v_fmamk_f32 v45, v110, 0xbb800000, v45
	v_fmac_f32_e32 v44, 0xbb800000, v110
	v_fmamk_f32 v41, v110, 0xbb800000, v41
	v_fmac_f32_e32 v40, 0xbb800000, v110
	v_pk_add_f32 v[108:109], s[0:1], v[108:109]
	v_readlane_b32 s2, v106, 16
	v_readlane_b32 s3, v106, 48
	v_pk_add_f32 v[112:113], v[140:141], v[138:139]
	v_pk_mul_f32 v[110:111], v[40:41], v[40:41]
	v_pk_mul_f32 v[138:139], v[44:45], v[44:45]
	v_add_f32_e32 v108, v108, v109
	v_readlane_b32 s0, v106, 0
	v_readlane_b32 s1, v106, 32
	v_mov_b32_e32 v106, s2
	v_mov_b32_e32 v107, s3
	v_pk_mov_b32 v[140:141], v[138:139], v[110:111] op_sel:[1,0]
	v_mov_b32_e32 v139, v111
	v_fmamk_f32 v39, v108, 0xbb800000, v39
	v_fmac_f32_e32 v38, 0xbb800000, v108
	v_fmamk_f32 v37, v108, 0xbb800000, v37
	v_fmac_f32_e32 v36, 0xbb800000, v108
	v_pk_add_f32 v[106:107], s[0:1], v[106:107]
	v_pk_add_f32 v[110:111], v[140:141], v[138:139]
	v_pk_mul_f32 v[108:109], v[36:37], v[36:37]
	v_pk_mul_f32 v[138:139], v[38:39], v[38:39]
	v_add_f32_e32 v106, v106, v107
	v_pk_mov_b32 v[140:141], v[138:139], v[108:109] op_sel:[1,0]
	v_mov_b32_e32 v139, v109
	v_fmamk_f32 v35, v106, 0xbb800000, v35
	v_fmac_f32_e32 v34, 0xbb800000, v106
	v_fmamk_f32 v31, v106, 0xbb800000, v31
	v_fmac_f32_e32 v30, 0xbb800000, v106
	v_pk_add_f32 v[108:109], v[140:141], v[138:139]
	v_pk_mul_f32 v[106:107], v[30:31], v[30:31]
	v_pk_mul_f32 v[138:139], v[34:35], v[34:35]
	v_add_f32_e32 v132, v132, v133
	v_pk_mov_b32 v[140:141], v[138:139], v[106:107] op_sel:[1,0]
	v_mov_b32_e32 v139, v107
	v_pk_add_f32 v[106:107], v[140:141], v[138:139]
	v_add_f32_e32 v122, v122, v123
	v_add_f32_e32 v133, v106, v107
	v_add_f32_dpp v106, v132, v132 quad_perm:[1,0,3,2] row_mask:0xf bank_mask:0xf bound_ctrl:1
	v_add_f32_e32 v123, v130, v131
	v_add_f32_e32 v131, v108, v109
	v_add_f32_dpp v106, v106, v106 quad_perm:[2,3,0,1] row_mask:0xf bank_mask:0xf bound_ctrl:1
	v_add_f32_e32 v118, v118, v119
	v_add_f32_e32 v130, v110, v111
	v_add_f32_dpp v106, v106, v106 row_half_mirror row_mask:0xf bank_mask:0xf bound_ctrl:1
	v_add_f32_e32 v119, v120, v121
	v_add_f32_e32 v120, v136, v137
	v_add_f32_dpp v106, v106, v106 row_mirror row_mask:0xf bank_mask:0xf bound_ctrl:1
	v_add_f32_e32 v128, v128, v129
	v_readlane_b32 s2, v106, 16
	v_readlane_b32 s3, v106, 48
	v_readlane_b32 s0, v106, 0
	v_readlane_b32 s1, v106, 32
	v_mov_b32_e32 v106, s2
	v_mov_b32_e32 v107, s3
	v_pk_add_f32 v[108:109], s[0:1], v[106:107]
	v_add_f32_dpp v106, v122, v122 quad_perm:[1,0,3,2] row_mask:0xf bank_mask:0xf bound_ctrl:1
	v_add_f32_e32 v129, v112, v113
	v_add_f32_dpp v112, v120, v120 quad_perm:[1,0,3,2] row_mask:0xf bank_mask:0xf bound_ctrl:1
	v_add_f32_dpp v106, v106, v106 quad_perm:[2,3,0,1] row_mask:0xf bank_mask:0xf bound_ctrl:1
	v_add_f32_e32 v121, v134, v135
	v_add_f32_dpp v112, v112, v112 quad_perm:[2,3,0,1] row_mask:0xf bank_mask:0xf bound_ctrl:1
	v_add_f32_dpp v106, v106, v106 row_half_mirror row_mask:0xf bank_mask:0xf bound_ctrl:1
	v_add_f32_e32 v126, v126, v127
	v_add_f32_dpp v112, v112, v112 row_half_mirror row_mask:0xf bank_mask:0xf bound_ctrl:1
	v_add_f32_dpp v106, v106, v106 row_mirror row_mask:0xf bank_mask:0xf bound_ctrl:1
	v_add_f32_e32 v127, v114, v115
	v_readlane_b32 s2, v106, 16
	v_readlane_b32 s3, v106, 48
	v_readlane_b32 s0, v106, 0
	v_readlane_b32 s1, v106, 32
	v_mov_b32_e32 v106, s2
	v_mov_b32_e32 v107, s3
	v_pk_add_f32 v[110:111], s[0:1], v[106:107]
	v_add_f32_dpp v106, v118, v118 quad_perm:[1,0,3,2] row_mask:0xf bank_mask:0xf bound_ctrl:1
	v_add_f32_dpp v112, v112, v112 row_mirror row_mask:0xf bank_mask:0xf bound_ctrl:1
	v_add_f32_dpp v114, v123, v123 quad_perm:[1,0,3,2] row_mask:0xf bank_mask:0xf bound_ctrl:1
	v_add_f32_dpp v106, v106, v106 quad_perm:[2,3,0,1] row_mask:0xf bank_mask:0xf bound_ctrl:1
	v_readlane_b32 s23, v112, 16
	v_readlane_b32 s24, v112, 48
	v_add_f32_dpp v106, v106, v106 row_half_mirror row_mask:0xf bank_mask:0xf bound_ctrl:1
	v_add_f32_dpp v114, v114, v114 quad_perm:[2,3,0,1] row_mask:0xf bank_mask:0xf bound_ctrl:1
	v_add_f32_e32 v124, v124, v125
	v_add_f32_dpp v106, v106, v106 row_mirror row_mask:0xf bank_mask:0xf bound_ctrl:1
	v_add_f32_dpp v114, v114, v114 row_half_mirror row_mask:0xf bank_mask:0xf bound_ctrl:1
	v_readlane_b32 s0, v106, 0
	v_readlane_b32 s2, v106, 16
	v_readlane_b32 s1, v106, 32
	v_readlane_b32 s3, v106, 48
	v_add_f32_dpp v106, v119, v119 quad_perm:[1,0,3,2] row_mask:0xf bank_mask:0xf bound_ctrl:1
	v_add_f32_dpp v114, v114, v114 row_mirror row_mask:0xf bank_mask:0xf bound_ctrl:1
	v_mov_b32_e32 v107, s3
	v_add_f32_dpp v106, v106, v106 quad_perm:[2,3,0,1] row_mask:0xf bank_mask:0xf bound_ctrl:1
	v_readlane_b32 s21, v114, 16
	v_readlane_b32 s22, v114, 48
	v_add_f32_dpp v106, v106, v106 row_half_mirror row_mask:0xf bank_mask:0xf bound_ctrl:1
	v_add_f32_e32 v125, v116, v117
	v_cvt_f32_f16_sdwa v115, v96 dst_sel:DWORD dst_unused:UNUSED_PAD src0_sel:WORD_1
	v_add_f32_dpp v106, v106, v106 row_mirror row_mask:0xf bank_mask:0xf bound_ctrl:1
	v_cvt_f32_f16_e32 v116, v97
	v_readlane_b32 s4, v106, 0
	v_readlane_b32 s6, v106, 16
	v_readlane_b32 s5, v106, 32
	v_readlane_b32 s7, v106, 48
	v_mov_b32_e32 v106, s2
	v_pk_add_f32 v[106:107], s[0:1], v[106:107]
	v_readlane_b32 s0, v112, 0
	v_readlane_b32 s1, v112, 32
	v_add_f32_dpp v112, v121, v121 quad_perm:[1,0,3,2] row_mask:0xf bank_mask:0xf bound_ctrl:1
	v_mov_b32_e32 v113, s7
	v_cvt_f32_f16_sdwa v117, v97 dst_sel:DWORD dst_unused:UNUSED_PAD src0_sel:WORD_1
	v_add_f32_dpp v112, v112, v112 quad_perm:[2,3,0,1] row_mask:0xf bank_mask:0xf bound_ctrl:1
	v_mov_b32_e32 v97, v108
	v_mov_b32_e32 v108, v111
	v_add_f32_dpp v112, v112, v112 row_half_mirror row_mask:0xf bank_mask:0xf bound_ctrl:1
	v_mov_b32_e32 v111, s24
	s_nop 0
	v_add_f32_dpp v112, v112, v112 row_mirror row_mask:0xf bank_mask:0xf bound_ctrl:1
	s_nop 0
	v_readlane_b32 s2, v112, 0
	v_readlane_b32 s19, v112, 16
	v_readlane_b32 s3, v112, 32
	v_readlane_b32 s20, v112, 48
	v_mov_b32_e32 v112, s6
	v_pk_add_f32 v[112:113], s[4:5], v[112:113]
	v_readlane_b32 s4, v114, 0
	v_readlane_b32 s5, v114, 32
	v_add_f32_dpp v114, v128, v128 quad_perm:[1,0,3,2] row_mask:0xf bank_mask:0xf bound_ctrl:1
	s_nop 1
	v_add_f32_dpp v114, v114, v114 quad_perm:[2,3,0,1] row_mask:0xf bank_mask:0xf bound_ctrl:1
	s_nop 1
	v_add_f32_dpp v114, v114, v114 row_half_mirror row_mask:0xf bank_mask:0xf bound_ctrl:1
	s_nop 1
	v_add_f32_dpp v114, v114, v114 row_mirror row_mask:0xf bank_mask:0xf bound_ctrl:1
	s_nop 0
	v_readlane_b32 s6, v114, 0
	v_readlane_b32 s29, v114, 16
	v_readlane_b32 s7, v114, 32
	v_readlane_b32 s30, v114, 48
	v_add_f32_dpp v114, v126, v126 quad_perm:[1,0,3,2] row_mask:0xf bank_mask:0xf bound_ctrl:1
	s_nop 1
	v_add_f32_dpp v114, v114, v114 quad_perm:[2,3,0,1] row_mask:0xf bank_mask:0xf bound_ctrl:1
	s_nop 1
	v_add_f32_dpp v114, v114, v114 row_half_mirror row_mask:0xf bank_mask:0xf bound_ctrl:1
	s_nop 1
	v_add_f32_dpp v114, v114, v114 row_mirror row_mask:0xf bank_mask:0xf bound_ctrl:1
	s_nop 0
	v_readlane_b32 s10, v114, 0
	v_readlane_b32 s31, v114, 16
	v_readlane_b32 s11, v114, 32
	v_readlane_b32 s33, v114, 48
	v_add_f32_dpp v114, v124, v124 quad_perm:[1,0,3,2] row_mask:0xf bank_mask:0xf bound_ctrl:1
	v_cvt_f32_f16_e32 v124, v69
	s_nop 0
	v_add_f32_dpp v114, v114, v114 quad_perm:[2,3,0,1] row_mask:0xf bank_mask:0xf bound_ctrl:1
	s_nop 1
	v_add_f32_dpp v114, v114, v114 row_half_mirror row_mask:0xf bank_mask:0xf bound_ctrl:1
	s_nop 1
	v_add_f32_dpp v114, v114, v114 row_mirror row_mask:0xf bank_mask:0xf bound_ctrl:1
	s_nop 0
	v_readlane_b32 s8, v114, 0
	v_readlane_b32 s34, v114, 16
	v_readlane_b32 s9, v114, 32
	v_readlane_b32 s35, v114, 48
	v_cvt_f32_f16_e32 v114, v96
	v_mov_b32_e32 v96, v110
	v_mov_b32_e32 v110, s23
	v_pk_add_f32 v[118:119], s[0:1], v[110:111]
	v_pk_add_f32 v[108:109], v[96:97], v[108:109]
	v_add_f32_dpp v110, v125, v125 quad_perm:[1,0,3,2] row_mask:0xf bank_mask:0xf bound_ctrl:1
	s_mov_b32 s0, 0x3b800000
	v_mov_b64_e32 v[96:97], s[28:29]
	v_add_f32_dpp v110, v110, v110 quad_perm:[2,3,0,1] row_mask:0xf bank_mask:0xf bound_ctrl:1
	v_cvt_f32_f16_sdwa v125, v69 dst_sel:DWORD dst_unused:UNUSED_PAD src0_sel:WORD_1
	v_mov_b32_e32 v69, v106
	v_add_f32_dpp v110, v110, v110 row_half_mirror row_mask:0xf bank_mask:0xf bound_ctrl:1
	v_mov_b32_e32 v106, v113
	s_nop 0
	v_add_f32_dpp v110, v110, v110 row_mirror row_mask:0xf bank_mask:0xf bound_ctrl:1
	s_nop 0
	v_readlane_b32 s24, v110, 0
	v_readlane_b32 s23, v110, 16
	v_readlane_b32 s25, v110, 32
	v_readlane_b32 s36, v110, 48
	v_add_f32_dpp v110, v127, v127 quad_perm:[1,0,3,2] row_mask:0xf bank_mask:0xf bound_ctrl:1
	s_nop 1
	v_add_f32_dpp v110, v110, v110 quad_perm:[2,3,0,1] row_mask:0xf bank_mask:0xf bound_ctrl:1
	s_nop 1
	v_add_f32_dpp v110, v110, v110 row_half_mirror row_mask:0xf bank_mask:0xf bound_ctrl:1
	s_nop 1
	v_add_f32_dpp v120, v110, v110 row_mirror row_mask:0xf bank_mask:0xf bound_ctrl:1
	v_pk_fma_f32 v[110:111], v[108:109], s[0:1], v[96:97] op_sel_hi:[1,0,0]
	s_mov_b32 s1, 0x800000
	v_mul_f32_e32 v108, 0x4b800000, v111
	v_cmp_gt_f32_e32 vcc, s1, v111
	v_readlane_b32 s26, v120, 0
	v_readlane_b32 s28, v120, 16
	v_cndmask_b32_e32 v108, v111, v108, vcc
	v_rsq_f32_e32 v108, v108
	v_readlane_b32 s27, v120, 32
	v_readlane_b32 s37, v120, 48
	v_mul_f32_e32 v109, 0x45800000, v108
	v_cndmask_b32_e32 v108, v108, v109, vcc
	v_pk_mul_f32 v[104:105], v[108:109], v[104:105] op_sel_hi:[0,1]
	v_pk_mul_f32 v[102:103], v[108:109], v[102:103] op_sel_hi:[0,1]
	v_pk_fma_f32 v[104:105], v[0:1], v[104:105], v[4:5]
	v_pk_fma_f32 v[102:103], v[2:3], v[102:103], v[6:7]
	v_pk_mul_f32 v[104:105], v[104:105], v[114:115]
	v_mov_b32_e32 v114, s19
	v_mov_b32_e32 v115, s20
	v_mov_b32_e32 v108, s21
	v_mov_b32_e32 v109, s22
	v_pk_mul_f32 v[102:103], v[102:103], v[116:117]
	v_pk_add_f32 v[120:121], s[2:3], v[114:115]
	v_pk_add_f32 v[114:115], s[4:5], v[108:109]
	v_mov_b32_e32 v108, s29
	v_mov_b32_e32 v109, s30
	v_cvt_pk_f16_f32 v104, v104, v105
	v_cvt_pk_f16_f32 v105, v102, v103
	v_mov_b32_e32 v102, s31
	v_mov_b32_e32 v103, s33
	v_pk_add_f32 v[116:117], s[6:7], v[108:109]
	v_pk_add_f32 v[108:109], s[10:11], v[102:103]
	v_add_f32_dpp v102, v129, v129 quad_perm:[1,0,3,2] row_mask:0xf bank_mask:0xf bound_ctrl:1
	v_cmp_gt_f32_e32 vcc, s1, v110
	v_mov_b32_e32 v103, s35
	v_add_f32_dpp v102, v102, v102 quad_perm:[2,3,0,1] row_mask:0xf bank_mask:0xf bound_ctrl:1
	global_store_dwordx2 v[60:61], v[104:105], off sc1
	v_mov_b32_e32 v105, s37
	v_add_f32_dpp v102, v102, v102 row_half_mirror row_mask:0xf bank_mask:0xf bound_ctrl:1
	s_nop 1
	v_add_f32_dpp v102, v102, v102 row_mirror row_mask:0xf bank_mask:0xf bound_ctrl:1
	s_nop 0
	v_readlane_b32 s2, v102, 0
	v_readlane_b32 s6, v102, 16
	v_readlane_b32 s3, v102, 32
	v_readlane_b32 s7, v102, 48
	v_mul_f32_e32 v102, 0x4b800000, v110
	v_cndmask_b32_e32 v122, v110, v102, vcc
	v_mov_b32_e32 v102, s34
	v_rsq_f32_e32 v122, v122
	v_pk_add_f32 v[110:111], s[8:9], v[102:103]
	v_add_f32_dpp v102, v130, v130 quad_perm:[1,0,3,2] row_mask:0xf bank_mask:0xf bound_ctrl:1
	v_cvt_f32_f16_sdwa v103, v70 dst_sel:DWORD dst_unused:UNUSED_PAD src0_sel:WORD_1
	v_mul_f32_e32 v104, 0x45800000, v122
	v_add_f32_dpp v102, v102, v102 quad_perm:[2,3,0,1] row_mask:0xf bank_mask:0xf bound_ctrl:1
	s_nop 1
	v_add_f32_dpp v102, v102, v102 row_half_mirror row_mask:0xf bank_mask:0xf bound_ctrl:1
	s_nop 1
	v_add_f32_dpp v102, v102, v102 row_mirror row_mask:0xf bank_mask:0xf bound_ctrl:1
	s_nop 0
	v_readlane_b32 s4, v102, 0
	v_readlane_b32 s8, v102, 16
	v_readlane_b32 s5, v102, 32
	v_readlane_b32 s9, v102, 48
	v_cvt_f32_f16_e32 v102, v70
	v_cndmask_b32_e32 v70, v122, v104, vcc
	v_pk_mul_f32 v[100:101], v[70:71], v[100:101] op_sel_hi:[0,1]
	v_pk_mul_f32 v[98:99], v[70:71], v[98:99] op_sel_hi:[0,1]
	v_cvt_f32_f16_e32 v70, v71
	v_cvt_f32_f16_sdwa v71, v71 dst_sel:DWORD dst_unused:UNUSED_PAD src0_sel:WORD_1
	v_pk_fma_f32 v[100:101], v[0:1], v[100:101], v[4:5]
	v_pk_fma_f32 v[98:99], v[2:3], v[98:99], v[6:7]
	v_pk_mul_f32 v[100:101], v[100:101], v[102:103]
	v_pk_mul_f32 v[70:71], v[98:99], v[70:71]
	v_cvt_pk_f16_f32 v100, v100, v101
	v_cvt_pk_f16_f32 v101, v70, v71
	v_cvt_f32_f16_e32 v70, v68
	v_cvt_f32_f16_sdwa v71, v68 dst_sel:DWORD dst_unused:UNUSED_PAD src0_sel:WORD_1
	v_mov_b32_e32 v68, v112
	v_pk_add_f32 v[68:69], v[68:69], v[106:107]
	v_add_f32_dpp v106, v131, v131 quad_perm:[1,0,3,2] row_mask:0xf bank_mask:0xf bound_ctrl:1
	v_mov_b32_e32 v98, s6
	v_mov_b32_e32 v99, s7
	v_add_f32_dpp v106, v106, v106 quad_perm:[2,3,0,1] row_mask:0xf bank_mask:0xf bound_ctrl:1
	v_pk_add_f32 v[98:99], s[2:3], v[98:99]
	v_add_co_u32_e32 v122, vcc, s18, v60
	v_add_f32_dpp v106, v106, v106 row_half_mirror row_mask:0xf bank_mask:0xf bound_ctrl:1
	s_nop 0
	v_addc_co_u32_e32 v123, vcc, 0, v61, vcc
	v_add_f32_dpp v106, v106, v106 row_mirror row_mask:0xf bank_mask:0xf bound_ctrl:1
	global_store_dwordx2 v[122:123], v[100:101], off offset:-4096 sc1
	v_readlane_b32 s2, v106, 0
	v_readlane_b32 s6, v106, 16
	v_readlane_b32 s3, v106, 32
	v_readlane_b32 s7, v106, 48
	v_add_f32_dpp v106, v133, v133 quad_perm:[1,0,3,2] row_mask:0xf bank_mask:0xf bound_ctrl:1
	v_mov_b32_e32 v100, s8
	v_mov_b32_e32 v101, s9
	v_add_f32_dpp v106, v106, v106 quad_perm:[2,3,0,1] row_mask:0xf bank_mask:0xf bound_ctrl:1
	v_pk_add_f32 v[100:101], s[4:5], v[100:101]
	v_mov_b32_e32 v102, s23
	v_add_f32_dpp v106, v106, v106 row_half_mirror row_mask:0xf bank_mask:0xf bound_ctrl:1
	v_mov_b32_e32 v103, s36
	v_mov_b32_e32 v104, s28
	v_add_f32_dpp v112, v106, v106 row_mirror row_mask:0xf bank_mask:0xf bound_ctrl:1
	v_pk_fma_f32 v[106:107], v[68:69], s[0:1], v[96:97] op_sel_hi:[1,0,0]
	v_readlane_b32 s4, v112, 0
	v_mul_f32_e32 v68, 0x4b800000, v107
	v_cmp_gt_f32_e32 vcc, s1, v107
	v_readlane_b32 s8, v112, 16
	v_readlane_b32 s5, v112, 32
	v_cndmask_b32_e32 v68, v107, v68, vcc
	v_rsq_f32_e32 v68, v68
	v_readlane_b32 s9, v112, 48
	v_pk_add_f32 v[102:103], s[24:25], v[102:103]
	v_pk_add_f32 v[104:105], s[26:27], v[104:105]
	v_mul_f32_e32 v69, 0x45800000, v68
	v_cndmask_b32_e32 v112, v68, v69, vcc
	v_pk_mul_f32 v[68:69], v[112:113], v[94:95] op_sel_hi:[0,1]
	v_pk_fma_f32 v[68:69], v[0:1], v[68:69], v[4:5]
	v_cmp_gt_f32_e32 vcc, s1, v106
	v_pk_mul_f32 v[94:95], v[68:69], v[70:71]
	v_mul_f32_e32 v70, 0x4b800000, v106
	v_cndmask_b32_e32 v106, v106, v70, vcc
	v_pk_mul_f32 v[92:93], v[112:113], v[92:93] op_sel_hi:[0,1]
	v_rsq_f32_e32 v106, v106
	v_pk_fma_f32 v[92:93], v[2:3], v[92:93], v[6:7]
	v_cvt_pk_f16_f32 v94, v94, v95
	v_pk_mul_f32 v[92:93], v[92:93], v[124:125]
	v_mov_b32_e32 v68, s6
	v_cvt_pk_f16_f32 v95, v92, v93
	global_store_dwordx2 v[122:123], v[94:95], off sc1
	v_mul_f32_e32 v94, 0x45800000, v106
	v_cvt_f32_f16_e32 v92, v42
	v_cvt_f32_f16_sdwa v93, v42 dst_sel:DWORD dst_unused:UNUSED_PAD src0_sel:WORD_1
	v_cndmask_b32_e32 v42, v106, v94, vcc
	v_pk_mul_f32 v[90:91], v[42:43], v[90:91] op_sel_hi:[0,1]
	v_pk_fma_f32 v[90:91], v[0:1], v[90:91], v[4:5]
	v_mov_b32_e32 v69, s7
	v_pk_mul_f32 v[90:91], v[90:91], v[92:93]
	v_cvt_f32_f16_e32 v92, v43
	v_cvt_f32_f16_sdwa v93, v43 dst_sel:DWORD dst_unused:UNUSED_PAD src0_sel:WORD_1
	v_pk_mul_f32 v[42:43], v[42:43], v[88:89] op_sel_hi:[0,1]
	v_pk_fma_f32 v[42:43], v[2:3], v[42:43], v[6:7]
	v_cvt_pk_f16_f32 v90, v90, v91
	v_pk_mul_f32 v[42:43], v[42:43], v[92:93]
	v_cvt_f32_f16_e32 v88, v32
	v_cvt_pk_f16_f32 v91, v42, v43
	v_add_co_u32_e32 v42, vcc, s17, v60
	v_mov_b32_e32 v70, s8
	s_nop 0
	v_addc_co_u32_e32 v43, vcc, 0, v61, vcc
	global_store_dwordx2 v[42:43], v[90:91], off offset:-4096 sc1
	v_mov_b32_e32 v90, v120
	v_mov_b32_e32 v91, v118
	v_mov_b32_e32 v118, v121
	v_pk_add_f32 v[90:91], v[90:91], v[118:119]
	v_mov_b32_e32 v71, s9
	v_pk_fma_f32 v[90:91], v[90:91], s[0:1], v[96:97] op_sel_hi:[1,0,0]
	v_pk_add_f32 v[68:69], s[2:3], v[68:69]
	v_mul_f32_e32 v89, 0x4b800000, v91
	v_cmp_gt_f32_e32 vcc, s1, v91
	v_pk_add_f32 v[70:71], s[4:5], v[70:71]
	s_nop 0
	v_cndmask_b32_e32 v89, v91, v89, vcc
	v_rsq_f32_e32 v91, v89
	v_cvt_f32_f16_sdwa v89, v32 dst_sel:DWORD dst_unused:UNUSED_PAD src0_sel:WORD_1
	v_cvt_f32_f16_e32 v32, v33
	v_cvt_f32_f16_sdwa v33, v33 dst_sel:DWORD dst_unused:UNUSED_PAD src0_sel:WORD_1
	v_mul_f32_e32 v92, 0x45800000, v91
	v_cndmask_b32_e32 v92, v91, v92, vcc
	v_pk_mul_f32 v[86:87], v[92:93], v[86:87] op_sel_hi:[0,1]
	v_pk_fma_f32 v[86:87], v[0:1], v[86:87], v[4:5]
	v_cmp_gt_f32_e32 vcc, s1, v90
	v_pk_mul_f32 v[86:87], v[86:87], v[88:89]
	v_pk_mul_f32 v[84:85], v[92:93], v[84:85] op_sel_hi:[0,1]
	v_cvt_pk_f16_f32 v86, v86, v87
	v_mul_f32_e32 v87, 0x4b800000, v90
	v_cndmask_b32_e32 v87, v90, v87, vcc
	v_rsq_f32_e32 v88, v87
	v_pk_fma_f32 v[84:85], v[2:3], v[84:85], v[6:7]
	s_nop 0
	v_pk_mul_f32 v[32:33], v[84:85], v[32:33]
	s_nop 0
	v_cvt_pk_f16_f32 v87, v32, v33
	global_store_dwordx2 v[42:43], v[86:87], off sc1
	v_mul_f32_e32 v42, 0x45800000, v88
	v_cvt_f32_f16_e32 v32, v28
	v_cvt_f32_f16_sdwa v33, v28 dst_sel:DWORD dst_unused:UNUSED_PAD src0_sel:WORD_1
	v_cndmask_b32_e32 v28, v88, v42, vcc
	v_pk_mul_f32 v[42:43], v[28:29], v[82:83] op_sel_hi:[0,1]
	v_pk_fma_f32 v[42:43], v[0:1], v[42:43], v[4:5]
	s_nop 0
	v_pk_mul_f32 v[32:33], v[42:43], v[32:33]
	v_cvt_f32_f16_e32 v42, v29
	v_cvt_f32_f16_sdwa v43, v29 dst_sel:DWORD dst_unused:UNUSED_PAD src0_sel:WORD_1
	v_pk_mul_f32 v[28:29], v[28:29], v[80:81] op_sel_hi:[0,1]
	v_pk_fma_f32 v[28:29], v[2:3], v[28:29], v[6:7]
	v_cvt_pk_f16_f32 v32, v32, v33
	v_pk_mul_f32 v[28:29], v[28:29], v[42:43]
	v_mov_b32_e32 v42, v116
	v_mov_b32_e32 v43, v114
	v_mov_b32_e32 v114, v117
	v_cvt_pk_f16_f32 v33, v28, v29
	v_add_co_u32_e32 v28, vcc, s16, v60
	v_pk_add_f32 v[42:43], v[42:43], v[114:115]
	s_nop 0
	v_addc_co_u32_e32 v29, vcc, 0, v61, vcc
	v_pk_fma_f32 v[42:43], v[42:43], s[0:1], v[96:97] op_sel_hi:[1,0,0]
	global_store_dwordx2 v[28:29], v[32:33], off offset:-4096 sc1
	v_mul_f32_e32 v33, 0x4b800000, v43
	v_cmp_gt_f32_e32 vcc, s1, v43
	v_cvt_f32_f16_e32 v32, v26
	s_nop 0
	v_cndmask_b32_e32 v33, v43, v33, vcc
	v_rsq_f32_e32 v43, v33
	v_cvt_f32_f16_sdwa v33, v26 dst_sel:DWORD dst_unused:UNUSED_PAD src0_sel:WORD_1
	v_cvt_f32_f16_e32 v26, v27
	v_cvt_f32_f16_sdwa v27, v27 dst_sel:DWORD dst_unused:UNUSED_PAD src0_sel:WORD_1
	v_mul_f32_e32 v80, 0x45800000, v43
	v_cndmask_b32_e32 v80, v43, v80, vcc
	v_pk_mul_f32 v[76:77], v[80:81], v[76:77] op_sel_hi:[0,1]
	v_pk_fma_f32 v[76:77], v[0:1], v[76:77], v[4:5]
	v_cmp_gt_f32_e32 vcc, s1, v42
	v_pk_mul_f32 v[32:33], v[76:77], v[32:33]
	v_pk_mul_f32 v[74:75], v[80:81], v[74:75] op_sel_hi:[0,1]
	v_cvt_pk_f16_f32 v32, v32, v33
	v_mul_f32_e32 v33, 0x4b800000, v42
	v_cndmask_b32_e32 v33, v42, v33, vcc
	v_rsq_f32_e32 v42, v33
	v_pk_fma_f32 v[74:75], v[2:3], v[74:75], v[6:7]
	s_nop 0
	v_pk_mul_f32 v[26:27], v[74:75], v[26:27]
	s_nop 0
	v_cvt_pk_f16_f32 v33, v26, v27
	global_store_dwordx2 v[28:29], v[32:33], off sc1
	v_mul_f32_e32 v28, 0x45800000, v42
	v_cvt_f32_f16_e32 v26, v24
	v_cvt_f32_f16_sdwa v27, v24 dst_sel:DWORD dst_unused:UNUSED_PAD src0_sel:WORD_1
	v_cndmask_b32_e32 v24, v42, v28, vcc
	v_pk_mul_f32 v[28:29], v[24:25], v[78:79] op_sel_hi:[0,1]
	v_pk_fma_f32 v[28:29], v[0:1], v[28:29], v[4:5]
	s_nop 0
	v_pk_mul_f32 v[26:27], v[28:29], v[26:27]
	v_cvt_f32_f16_e32 v28, v25
	v_cvt_f32_f16_sdwa v29, v25 dst_sel:DWORD dst_unused:UNUSED_PAD src0_sel:WORD_1
	v_pk_mul_f32 v[24:25], v[24:25], v[72:73] op_sel_hi:[0,1]
	v_pk_fma_f32 v[24:25], v[2:3], v[24:25], v[6:7]
	v_cvt_pk_f16_f32 v26, v26, v27
	v_pk_mul_f32 v[24:25], v[24:25], v[28:29]
	v_mov_b32_e32 v28, v110
	v_mov_b32_e32 v29, v108
	v_mov_b32_e32 v108, v111
	v_cvt_pk_f16_f32 v27, v24, v25
	v_add_co_u32_e32 v24, vcc, s15, v60
	v_pk_add_f32 v[28:29], v[28:29], v[108:109]
	s_nop 0
	v_addc_co_u32_e32 v25, vcc, 0, v61, vcc
	v_pk_fma_f32 v[28:29], v[28:29], s[0:1], v[96:97] op_sel_hi:[1,0,0]
	global_store_dwordx2 v[24:25], v[26:27], off offset:-4096 sc1
	v_mul_f32_e32 v27, 0x4b800000, v29
	v_cmp_gt_f32_e32 vcc, s1, v29
	v_cvt_f32_f16_e32 v26, v22
	s_nop 0
	v_cndmask_b32_e32 v27, v29, v27, vcc
	v_rsq_f32_e32 v29, v27
	v_cvt_f32_f16_sdwa v27, v22 dst_sel:DWORD dst_unused:UNUSED_PAD src0_sel:WORD_1
	v_cvt_f32_f16_e32 v22, v23
	v_cvt_f32_f16_sdwa v23, v23 dst_sel:DWORD dst_unused:UNUSED_PAD src0_sel:WORD_1
	v_mul_f32_e32 v32, 0x45800000, v29
	v_cndmask_b32_e32 v32, v29, v32, vcc
	v_pk_mul_f32 v[42:43], v[32:33], v[66:67] op_sel_hi:[0,1]
	v_pk_fma_f32 v[42:43], v[0:1], v[42:43], v[4:5]
	v_cmp_gt_f32_e32 vcc, s1, v28
	v_pk_mul_f32 v[26:27], v[42:43], v[26:27]
	v_pk_mul_f32 v[32:33], v[32:33], v[64:65] op_sel_hi:[0,1]
	v_cvt_pk_f16_f32 v26, v26, v27
	v_mul_f32_e32 v27, 0x4b800000, v28
	v_cndmask_b32_e32 v27, v28, v27, vcc
	v_rsq_f32_e32 v28, v27
	v_pk_fma_f32 v[32:33], v[2:3], v[32:33], v[6:7]
	s_nop 0
	v_pk_mul_f32 v[22:23], v[32:33], v[22:23]
	s_nop 0
	v_cvt_pk_f16_f32 v27, v22, v23
	global_store_dwordx2 v[24:25], v[26:27], off sc1
	v_mul_f32_e32 v24, 0x45800000, v28
	v_cvt_f32_f16_e32 v22, v20
	v_cvt_f32_f16_sdwa v23, v20 dst_sel:DWORD dst_unused:UNUSED_PAD src0_sel:WORD_1
	v_cndmask_b32_e32 v20, v28, v24, vcc
	v_pk_mul_f32 v[24:25], v[20:21], v[62:63] op_sel_hi:[0,1]
	v_pk_fma_f32 v[24:25], v[0:1], v[24:25], v[4:5]
	s_nop 0
	v_pk_mul_f32 v[22:23], v[24:25], v[22:23]
	v_cvt_f32_f16_e32 v24, v21
	v_cvt_f32_f16_sdwa v25, v21 dst_sel:DWORD dst_unused:UNUSED_PAD src0_sel:WORD_1
	v_pk_mul_f32 v[20:21], v[20:21], v[58:59] op_sel_hi:[0,1]
	v_pk_fma_f32 v[20:21], v[2:3], v[20:21], v[6:7]
	v_cvt_pk_f16_f32 v22, v22, v23
	v_pk_mul_f32 v[20:21], v[20:21], v[24:25]
	v_mov_b32_e32 v24, v104
	v_mov_b32_e32 v25, v102
	v_mov_b32_e32 v102, v105
	v_cvt_pk_f16_f32 v23, v20, v21
	v_add_co_u32_e32 v20, vcc, s14, v60
	v_pk_add_f32 v[24:25], v[24:25], v[102:103]
	s_nop 0
	v_addc_co_u32_e32 v21, vcc, 0, v61, vcc
	v_pk_fma_f32 v[24:25], v[24:25], s[0:1], v[96:97] op_sel_hi:[1,0,0]
	global_store_dwordx2 v[20:21], v[22:23], off offset:-4096 sc1
	v_mul_f32_e32 v23, 0x4b800000, v25
	v_cmp_gt_f32_e32 vcc, s1, v25
	v_cvt_f32_f16_e32 v22, v18
	s_nop 0
	v_cndmask_b32_e32 v23, v25, v23, vcc
	v_rsq_f32_e32 v25, v23
	v_cvt_f32_f16_sdwa v23, v18 dst_sel:DWORD dst_unused:UNUSED_PAD src0_sel:WORD_1
	v_cvt_f32_f16_e32 v18, v19
	v_cvt_f32_f16_sdwa v19, v19 dst_sel:DWORD dst_unused:UNUSED_PAD src0_sel:WORD_1
	v_mul_f32_e32 v26, 0x45800000, v25
	v_cndmask_b32_e32 v26, v25, v26, vcc
	v_pk_mul_f32 v[28:29], v[26:27], v[54:55] op_sel_hi:[0,1]
	v_pk_fma_f32 v[28:29], v[0:1], v[28:29], v[4:5]
	v_cmp_gt_f32_e32 vcc, s1, v24
	v_pk_mul_f32 v[22:23], v[28:29], v[22:23]
	v_pk_mul_f32 v[26:27], v[26:27], v[52:53] op_sel_hi:[0,1]
	v_cvt_pk_f16_f32 v22, v22, v23
	v_mul_f32_e32 v23, 0x4b800000, v24
	v_cndmask_b32_e32 v23, v24, v23, vcc
	v_rsq_f32_e32 v24, v23
	v_pk_fma_f32 v[26:27], v[2:3], v[26:27], v[6:7]
	s_nop 0
	v_pk_mul_f32 v[18:19], v[26:27], v[18:19]
	s_nop 0
	v_cvt_pk_f16_f32 v23, v18, v19
	global_store_dwordx2 v[20:21], v[22:23], off sc1
	v_mul_f32_e32 v20, 0x45800000, v24
	v_cvt_f32_f16_e32 v18, v16
	v_cvt_f32_f16_sdwa v19, v16 dst_sel:DWORD dst_unused:UNUSED_PAD src0_sel:WORD_1
	v_cndmask_b32_e32 v16, v24, v20, vcc
	v_pk_mul_f32 v[20:21], v[16:17], v[56:57] op_sel_hi:[0,1]
	v_pk_fma_f32 v[20:21], v[0:1], v[20:21], v[4:5]
	s_nop 0
	v_pk_mul_f32 v[18:19], v[20:21], v[18:19]
	v_cvt_f32_f16_e32 v20, v17
	v_cvt_f32_f16_sdwa v21, v17 dst_sel:DWORD dst_unused:UNUSED_PAD src0_sel:WORD_1
	v_pk_mul_f32 v[16:17], v[16:17], v[50:51] op_sel_hi:[0,1]
	v_pk_fma_f32 v[16:17], v[2:3], v[16:17], v[6:7]
	v_cvt_pk_f16_f32 v18, v18, v19
	v_pk_mul_f32 v[16:17], v[16:17], v[20:21]
	v_mov_b32_e32 v20, v100
	v_mov_b32_e32 v21, v98
	v_mov_b32_e32 v98, v101
	v_cvt_pk_f16_f32 v19, v16, v17
	v_add_co_u32_e32 v16, vcc, s13, v60
	v_pk_add_f32 v[20:21], v[20:21], v[98:99]
	s_nop 0
	v_addc_co_u32_e32 v17, vcc, 0, v61, vcc
	v_pk_fma_f32 v[20:21], v[20:21], s[0:1], v[96:97] op_sel_hi:[1,0,0]
	global_store_dwordx2 v[16:17], v[18:19], off offset:-4096 sc1
	v_mul_f32_e32 v19, 0x4b800000, v21
	v_cmp_gt_f32_e32 vcc, s1, v21
	v_cvt_f32_f16_e32 v18, v14
	s_nop 0
	v_cndmask_b32_e32 v19, v21, v19, vcc
	v_rsq_f32_e32 v21, v19
	v_cvt_f32_f16_sdwa v19, v14 dst_sel:DWORD dst_unused:UNUSED_PAD src0_sel:WORD_1
	v_cvt_f32_f16_e32 v14, v15
	v_cvt_f32_f16_sdwa v15, v15 dst_sel:DWORD dst_unused:UNUSED_PAD src0_sel:WORD_1
	v_mul_f32_e32 v22, 0x45800000, v21
	v_cndmask_b32_e32 v22, v21, v22, vcc
	v_pk_mul_f32 v[24:25], v[22:23], v[48:49] op_sel_hi:[0,1]
	v_pk_fma_f32 v[24:25], v[0:1], v[24:25], v[4:5]
	v_cmp_gt_f32_e32 vcc, s1, v20
	v_pk_mul_f32 v[18:19], v[24:25], v[18:19]
	v_pk_mul_f32 v[22:23], v[22:23], v[46:47] op_sel_hi:[0,1]
	v_cvt_pk_f16_f32 v18, v18, v19
	v_mul_f32_e32 v19, 0x4b800000, v20
	v_cndmask_b32_e32 v19, v20, v19, vcc
	v_rsq_f32_e32 v20, v19
	v_pk_fma_f32 v[22:23], v[2:3], v[22:23], v[6:7]
	s_nop 0
	v_pk_mul_f32 v[14:15], v[22:23], v[14:15]
	s_nop 0
	v_cvt_pk_f16_f32 v19, v14, v15
	global_store_dwordx2 v[16:17], v[18:19], off sc1
	v_mul_f32_e32 v16, 0x45800000, v20
	v_cvt_f32_f16_e32 v14, v12
	v_cvt_f32_f16_sdwa v15, v12 dst_sel:DWORD dst_unused:UNUSED_PAD src0_sel:WORD_1
	v_cndmask_b32_e32 v12, v20, v16, vcc
	v_pk_mul_f32 v[16:17], v[12:13], v[44:45] op_sel_hi:[0,1]
	v_pk_fma_f32 v[16:17], v[0:1], v[16:17], v[4:5]
	s_nop 0
	v_pk_mul_f32 v[14:15], v[16:17], v[14:15]
	v_cvt_f32_f16_e32 v16, v13
	v_cvt_f32_f16_sdwa v17, v13 dst_sel:DWORD dst_unused:UNUSED_PAD src0_sel:WORD_1
	v_pk_mul_f32 v[12:13], v[12:13], v[40:41] op_sel_hi:[0,1]
	v_pk_fma_f32 v[12:13], v[2:3], v[12:13], v[6:7]
	v_cvt_pk_f16_f32 v14, v14, v15
	v_pk_mul_f32 v[12:13], v[12:13], v[16:17]
	v_mov_b32_e32 v16, v70
	v_mov_b32_e32 v17, v68
	v_mov_b32_e32 v68, v71
	v_cvt_pk_f16_f32 v15, v12, v13
	v_add_co_u32_e32 v12, vcc, s12, v60
	v_pk_add_f32 v[16:17], v[16:17], v[68:69]
	s_nop 0
	v_addc_co_u32_e32 v13, vcc, 0, v61, vcc
	v_pk_fma_f32 v[16:17], v[16:17], s[0:1], v[96:97] op_sel_hi:[1,0,0]
	global_store_dwordx2 v[12:13], v[14:15], off offset:-4096 sc1
	v_mul_f32_e32 v15, 0x4b800000, v17
	v_cmp_gt_f32_e32 vcc, s1, v17
	v_cvt_f32_f16_e32 v14, v10
	s_nop 0
	v_cndmask_b32_e32 v15, v17, v15, vcc
	v_rsq_f32_e32 v17, v15
	v_cvt_f32_f16_sdwa v15, v10 dst_sel:DWORD dst_unused:UNUSED_PAD src0_sel:WORD_1
	v_cvt_f32_f16_e32 v10, v11
	v_cvt_f32_f16_sdwa v11, v11 dst_sel:DWORD dst_unused:UNUSED_PAD src0_sel:WORD_1
	v_mul_f32_e32 v18, 0x45800000, v17
	v_cndmask_b32_e32 v18, v17, v18, vcc
	v_pk_mul_f32 v[20:21], v[18:19], v[38:39] op_sel_hi:[0,1]
	v_pk_fma_f32 v[20:21], v[0:1], v[20:21], v[4:5]
	v_cmp_gt_f32_e32 vcc, s1, v16
	v_pk_mul_f32 v[14:15], v[20:21], v[14:15]
	v_pk_mul_f32 v[18:19], v[18:19], v[36:37] op_sel_hi:[0,1]
	v_cvt_pk_f16_f32 v14, v14, v15
	v_mul_f32_e32 v15, 0x4b800000, v16
	v_cndmask_b32_e32 v15, v16, v15, vcc
	v_rsq_f32_e32 v16, v15
	v_pk_fma_f32 v[18:19], v[2:3], v[18:19], v[6:7]
	s_nop 0
	v_pk_mul_f32 v[10:11], v[18:19], v[10:11]
	s_nop 0
	v_cvt_pk_f16_f32 v15, v10, v11
	global_store_dwordx2 v[12:13], v[14:15], off sc1
	v_mul_f32_e32 v12, 0x45800000, v16
	v_cvt_f32_f16_e32 v10, v8
	v_cvt_f32_f16_sdwa v11, v8 dst_sel:DWORD dst_unused:UNUSED_PAD src0_sel:WORD_1
	v_cndmask_b32_e32 v8, v16, v12, vcc
	v_pk_mul_f32 v[12:13], v[8:9], v[34:35] op_sel_hi:[0,1]
	v_pk_fma_f32 v[0:1], v[0:1], v[12:13], v[4:5]
	v_cvt_f32_f16_e32 v4, v9
	v_cvt_f32_f16_sdwa v5, v9 dst_sel:DWORD dst_unused:UNUSED_PAD src0_sel:WORD_1
	v_pk_mul_f32 v[8:9], v[8:9], v[30:31] op_sel_hi:[0,1]
	v_pk_fma_f32 v[2:3], v[2:3], v[8:9], v[6:7]
	v_pk_mul_f32 v[0:1], v[0:1], v[10:11]
	v_pk_mul_f32 v[2:3], v[2:3], v[4:5]
	v_cvt_pk_f16_f32 v0, v0, v1
	v_cvt_pk_f16_f32 v1, v2, v3
	v_add_co_u32_e32 v2, vcc, 0xf000, v60
	s_nop 1
	v_addc_co_u32_e32 v3, vcc, 0, v61, vcc
	global_store_dwordx2 v[2:3], v[0:1], off sc1
	s_endpgm
	.p2align	8

.LBB2_4:
	s_waitcnt lgkmcnt(0)
	s_cmp_lg_u64 s[12:13], 0
	s_cselect_b64 s[20:21], -1, 0
	s_cmp_eq_u64 s[12:13], 0
	s_cbranch_scc1 .LBB2_6
	v_lshl_add_u64 v[6:7], v[6:7], 2, s[12:13]
	s_waitcnt vmcnt(0)
	global_store_dwordx4 v[6:7], v[2:5], off sc1

.LBB2_10:
	s_load_dwordx2 s[8:9], s[0:1], 0x28
	s_andn2_b64 vcc, exec, s[20:21]
	s_cbranch_vccnz .LBB2_12
	v_lshl_add_u64 v[12:13], v[14:15], 2, s[12:13]
	s_waitcnt vmcnt(0)
	global_store_dwordx4 v[12:13], v[6:9], off sc1

.LBB2_17:
	s_or_b64 exec, exec, s[0:1]
	s_waitcnt lgkmcnt(0)
	v_lshl_add_u64 v[8:9], s[4:5], 0, v[10:11]
	s_movk_i32 s0, 0x1000
	v_add_co_u32_e32 v8, vcc, s0, v8
	v_lshl_add_u64 v[16:17], s[6:7], 0, v[10:11]
	s_nop 0
	v_addc_co_u32_e32 v9, vcc, 0, v9, vcc
	s_barrier
	global_load_dwordx4 v[12:15], v10, s[4:5]
	global_load_dwordx4 v[20:23], v10, s[6:7]
	global_load_dwordx4 v[24:27], v[8:9], off
	v_add_co_u32_e32 v8, vcc, s0, v16
	v_mov_b32_e32 v16, 0x3727c5ac
	s_nop 0
	v_addc_co_u32_e32 v9, vcc, 0, v17, vcc
	global_load_dwordx4 v[28:31], v[8:9], off
	ds_read_b128 v[8:11], v11
	s_mov_b32 s4, 0x800000
	s_lshl_b64 s[0:1], s[2:3], 12
	s_add_u32 s0, s8, s0
	s_addc_u32 s1, s9, s1
	s_waitcnt lgkmcnt(0)
	v_add_f32_e32 v8, v8, v9
	v_add_f32_e32 v8, v8, v10
	v_add_f32_e32 v8, v8, v11
	v_fmac_f32_e32 v16, 0x3a000000, v8
	v_mul_f32_e32 v8, 0x4b800000, v16
	v_cmp_gt_f32_e32 vcc, s4, v16
	v_lshlrev_b32_e32 v9, 1, v18
	s_nop 0
	v_cndmask_b32_e32 v8, v16, v8, vcc
	v_rsq_f32_e32 v8, v8
	s_nop 0
	v_mul_f32_e32 v10, 0x45800000, v8
	v_cndmask_b32_e32 v8, v8, v10, vcc
	v_pk_mul_f32 v[0:1], v[8:9], v[0:1] op_sel_hi:[0,1]
	v_pk_mul_f32 v[2:3], v[8:9], v[2:3] op_sel_hi:[0,1]
	v_pk_mul_f32 v[4:5], v[8:9], v[4:5] op_sel_hi:[0,1]
	v_pk_mul_f32 v[6:7], v[8:9], v[6:7] op_sel_hi:[0,1]
	s_waitcnt vmcnt(2)
	v_pk_fma_f32 v[0:1], v[12:13], v[0:1], v[20:21]
	v_pk_fma_f32 v[2:3], v[14:15], v[2:3], v[22:23]
	v_cvt_pk_f16_f32 v0, v0, v1
	v_cvt_pk_f16_f32 v1, v2, v3
	global_store_dwordx2 v9, v[0:1], s[0:1] sc1
	s_waitcnt vmcnt(1)
	v_pk_fma_f32 v[0:1], v[24:25], v[4:5], v[28:29]
	v_pk_fma_f32 v[2:3], v[26:27], v[6:7], v[30:31]
	v_cvt_pk_f16_f32 v0, v0, v1
	v_cvt_pk_f16_f32 v1, v2, v3
	global_store_dwordx2 v9, v[0:1], s[0:1] offset:2048 sc1

.LBB3_4:
	s_waitcnt lgkmcnt(0)
	s_cmp_lg_u64 s[16:17], 0
	s_cselect_b64 s[14:15], -1, 0
	s_cmp_eq_u64 s[16:17], 0
	v_lshl_add_u64 v[20:21], v[14:15], 1, s[16:17]
	s_cbranch_scc1 .LBB3_6
	v_cvt_f16_f32_e32 v1, v2
	v_cvt_f16_f32_e32 v8, v3
	v_cvt_f16_f32_e32 v9, v4
	v_cvt_f16_f32_e32 v14, v5
	v_cvt_pk_f16_f32 v7, v4, v5
	v_cvt_pk_f16_f32 v6, v2, v3
	v_cvt_f32_f16_e32 v2, v1
	v_cvt_f32_f16_e32 v3, v8
	v_cvt_f32_f16_e32 v4, v9
	v_cvt_f32_f16_e32 v5, v14
	global_store_dwordx2 v[20:21], v[6:7], off sc1

.LBB3_10:
	s_load_dwordx2 s[8:9], s[0:1], 0x28
	v_mov_b32_e32 v17, v23
	s_andn2_b64 vcc, exec, s[14:15]
	s_cbranch_vccnz .LBB3_12
	v_cvt_f16_f32_e32 v8, v22
	v_cvt_f16_f32_e32 v9, v23
	v_cvt_f16_f32_e32 v1, v24
	v_cvt_f16_f32_e32 v7, v25
	v_cvt_f32_f16_e32 v8, v8
	v_cvt_f32_f16_e32 v9, v9
	v_cvt_f32_f16_e32 v6, v1
	v_cvt_f32_f16_e32 v7, v7
	v_cvt_pk_f16_f32 v11, v22, v23
	v_cvt_pk_f16_f32 v10, v24, v25
	global_store_dwordx2 v[20:21], v[10:11], off offset:2048 sc1
	v_mov_b64_e32 v[16:17], v[8:9]
	v_mov_b64_e32 v[14:15], v[6:7]
	v_mov_b64_e32 v[12:13], v[4:5]
	v_mov_b64_e32 v[10:11], v[2:3]
	v_mov_b32_e32 v24, v6
	v_mov_b32_e32 v25, v7
	v_mov_b32_e32 v22, v8
	v_mov_b32_e32 v23, v9

.LBB3_17:
	s_or_b64 exec, exec, s[0:1]
	v_lshl_add_u64 v[16:17], s[4:5], 0, v[18:19]
	s_movk_i32 s0, 0x1000
	v_add_co_u32_e32 v16, vcc, s0, v16
	v_lshl_add_u64 v[24:25], s[6:7], 0, v[18:19]
	s_nop 0
	v_addc_co_u32_e32 v17, vcc, 0, v17, vcc
	s_waitcnt lgkmcnt(0)
	s_barrier
	global_load_dwordx4 v[8:11], v18, s[4:5]
	global_load_dwordx4 v[12:15], v18, s[6:7]
	global_load_dwordx4 v[20:23], v[16:17], off
	v_add_co_u32_e32 v16, vcc, s0, v24
	v_mov_b32_e32 v24, 0x3727c5ac
	s_nop 0
	v_addc_co_u32_e32 v17, vcc, 0, v25, vcc
	global_load_dwordx4 v[28:31], v[16:17], off
	ds_read_b128 v[16:19], v19
	s_mov_b32 s4, 0x800000
	s_lshl_b64 s[0:1], s[2:3], 12
	s_add_u32 s0, s8, s0
	s_addc_u32 s1, s9, s1
	s_waitcnt lgkmcnt(0)
	v_add_f32_e32 v16, v16, v17
	v_add_f32_e32 v16, v16, v18
	v_add_f32_e32 v16, v16, v19
	v_fmac_f32_e32 v24, 0x3a000000, v16
	v_mul_f32_e32 v16, 0x4b800000, v24
	v_cmp_gt_f32_e32 vcc, s4, v24
	v_lshlrev_b32_e32 v17, 1, v26
	s_nop 0
	v_cndmask_b32_e32 v16, v24, v16, vcc
	v_rsq_f32_e32 v16, v16
	s_nop 0
	v_mul_f32_e32 v18, 0x45800000, v16
	v_cndmask_b32_e32 v16, v16, v18, vcc
	v_pk_mul_f32 v[0:1], v[16:17], v[0:1] op_sel_hi:[0,1]
	v_pk_mul_f32 v[2:3], v[16:17], v[2:3] op_sel_hi:[0,1]
	v_pk_mul_f32 v[4:5], v[16:17], v[4:5] op_sel_hi:[0,1]
	v_pk_mul_f32 v[6:7], v[16:17], v[6:7] op_sel_hi:[0,1]
	s_waitcnt vmcnt(2)
	v_pk_fma_f32 v[0:1], v[8:9], v[0:1], v[12:13]
	v_pk_fma_f32 v[2:3], v[10:11], v[2:3], v[14:15]
	v_cvt_pk_f16_f32 v0, v0, v1
	v_cvt_pk_f16_f32 v1, v2, v3
	global_store_dwordx2 v17, v[0:1], s[0:1] sc1
	s_waitcnt vmcnt(1)
	v_pk_fma_f32 v[0:1], v[20:21], v[4:5], v[28:29]
	v_pk_fma_f32 v[2:3], v[22:23], v[6:7], v[30:31]
	v_cvt_pk_f16_f32 v0, v0, v1
	v_cvt_pk_f16_f32 v1, v2, v3
	global_store_dwordx2 v17, v[0:1], s[0:1] offset:2048 sc1

.LBB6_4:
	s_waitcnt lgkmcnt(0)
	s_cmp_lg_u64 s[20:21], 0
	s_cselect_b64 s[18:19], -1, 0
	s_cmp_eq_u64 s[20:21], 0
	v_lshl_add_u64 v[24:25], v[12:13], 1, s[20:21]
	s_cbranch_scc1 .LBB6_6
	s_waitcnt vmcnt(0)
	v_cvt_f16_f32_e32 v1, v2
	v_cvt_f16_f32_e32 v8, v3
	v_cvt_f16_f32_e32 v9, v4
	v_cvt_f16_f32_e32 v12, v5
	v_cvt_pk_f16_f32 v7, v4, v5
	v_cvt_pk_f16_f32 v6, v2, v3
	v_cvt_f32_f16_e32 v2, v1
	v_cvt_f32_f16_e32 v3, v8
	v_cvt_f32_f16_e32 v4, v9
	v_cvt_f32_f16_e32 v5, v12
	global_store_dwordx2 v[24:25], v[6:7], off sc1

.LBB6_10:
	s_load_dwordx2 s[8:9], s[0:1], 0x28
	v_mov_b32_e32 v17, v21
	s_andn2_b64 vcc, exec, s[18:19]
	s_cbranch_vccnz .LBB6_12
	v_cvt_f16_f32_e32 v8, v20
	v_cvt_f16_f32_e32 v9, v21
	v_cvt_f16_f32_e32 v1, v18
	v_cvt_f16_f32_e32 v7, v19
	v_cvt_f32_f16_e32 v8, v8
	v_cvt_f32_f16_e32 v9, v9
	v_cvt_f32_f16_e32 v6, v1
	v_cvt_f32_f16_e32 v7, v7
	v_cvt_pk_f16_f32 v11, v20, v21
	v_cvt_pk_f16_f32 v10, v18, v19
	global_store_dwordx2 v[24:25], v[10:11], off offset:2048 sc1
	v_mov_b64_e32 v[16:17], v[8:9]
	v_mov_b64_e32 v[14:15], v[6:7]
	v_mov_b64_e32 v[12:13], v[4:5]
	v_mov_b64_e32 v[10:11], v[2:3]
	v_mov_b32_e32 v18, v6
	v_mov_b32_e32 v19, v7
	v_mov_b32_e32 v20, v8
	v_mov_b32_e32 v21, v9

.LBB6_17:
	s_or_b64 exec, exec, s[0:1]
	v_lshl_add_u64 v[16:17], s[4:5], 0, v[22:23]
	s_movk_i32 s0, 0x1000
	v_add_co_u32_e32 v16, vcc, s0, v16
	v_lshl_add_u64 v[20:21], s[6:7], 0, v[22:23]
	s_nop 0
	v_addc_co_u32_e32 v17, vcc, 0, v17, vcc
	s_waitcnt lgkmcnt(0)
	s_barrier
	global_load_dwordx4 v[8:11], v22, s[4:5]
	global_load_dwordx4 v[12:15], v22, s[6:7]
	v_add_co_u32_e32 v20, vcc, s0, v20
	global_load_dwordx4 v[16:19], v[16:17], off
	s_nop 0
	v_addc_co_u32_e32 v21, vcc, 0, v21, vcc
	global_load_dwordx4 v[24:27], v[20:21], off
	ds_read_b128 v[20:23], v23
	v_mov_b32_e32 v29, 0x3727c5ac
	s_mov_b32 s4, 0x800000
	s_lshl_b64 s[0:1], s[2:3], 12
	s_add_u32 s0, s8, s0
	s_waitcnt lgkmcnt(0)
	v_add_f32_e32 v20, v20, v21
	v_add_f32_e32 v20, v20, v22
	v_add_f32_e32 v20, v20, v23
	v_fmac_f32_e32 v29, 0x3a000000, v20
	v_mul_f32_e32 v20, 0x4b800000, v29
	v_cmp_gt_f32_e32 vcc, s4, v29
	v_lshlrev_b32_e32 v21, 1, v28
	s_addc_u32 s1, s9, s1
	v_cndmask_b32_e32 v20, v29, v20, vcc
	v_rsq_f32_e32 v20, v20
	s_nop 0
	v_mul_f32_e32 v22, 0x45800000, v20
	v_cndmask_b32_e32 v20, v20, v22, vcc
	v_pk_mul_f32 v[0:1], v[20:21], v[0:1] op_sel_hi:[0,1]
	v_pk_mul_f32 v[2:3], v[20:21], v[2:3] op_sel_hi:[0,1]
	v_pk_mul_f32 v[4:5], v[20:21], v[4:5] op_sel_hi:[0,1]
	v_pk_mul_f32 v[6:7], v[20:21], v[6:7] op_sel_hi:[0,1]
	s_waitcnt vmcnt(2)
	v_pk_fma_f32 v[0:1], v[8:9], v[0:1], v[12:13]
	v_pk_fma_f32 v[2:3], v[10:11], v[2:3], v[14:15]
	v_cvt_pk_f16_f32 v0, v0, v1
	v_cvt_pk_f16_f32 v1, v2, v3
	global_store_dwordx2 v21, v[0:1], s[0:1] sc1
	s_waitcnt vmcnt(1)
	v_pk_fma_f32 v[0:1], v[16:17], v[4:5], v[24:25]
	v_pk_fma_f32 v[2:3], v[18:19], v[6:7], v[26:27]
	v_cvt_pk_f16_f32 v0, v0, v1
	v_cvt_pk_f16_f32 v1, v2, v3
	global_store_dwordx2 v21, v[0:1], s[0:1] offset:2048 sc1

.LBB8_4:
	s_waitcnt lgkmcnt(0)
	s_cmp_lg_u64 s[4:5], 0
	s_cselect_b64 s[18:19], -1, 0
	s_cmp_eq_u64 s[4:5], 0
	s_cbranch_scc1 .LBB8_6
	v_lshl_add_u64 v[8:9], v[8:9], 2, s[4:5]
	global_store_dwordx4 v[8:9], v[2:5], off sc1

.LBB8_10:
	s_load_dwordx2 s[8:9], s[0:1], 0x28
	s_andn2_b64 vcc, exec, s[18:19]
	s_cbranch_vccnz .LBB8_12
	v_lshl_add_u64 v[12:13], s[12:13], 0, v[12:13]
	v_lshl_add_u64 v[12:13], v[12:13], 2, s[4:5]
	global_store_dwordx4 v[12:13], v[6:9], off sc1

.LBB8_17:
	s_or_b64 exec, exec, s[0:1]
	s_waitcnt lgkmcnt(0)
	v_lshl_add_u64 v[8:9], s[4:5], 0, v[10:11]
	s_movk_i32 s0, 0x1000
	v_add_co_u32_e32 v8, vcc, s0, v8
	v_lshl_add_u64 v[12:13], s[6:7], 0, v[10:11]
	s_nop 0
	v_addc_co_u32_e32 v9, vcc, 0, v9, vcc
	s_barrier
	global_load_dwordx4 v[16:19], v10, s[4:5]
	global_load_dwordx4 v[20:23], v10, s[6:7]
	global_load_dwordx4 v[24:27], v[8:9], off
	v_add_co_u32_e32 v8, vcc, s0, v12
	v_mov_b32_e32 v12, 0x3727c5ac
	s_nop 0
	v_addc_co_u32_e32 v9, vcc, 0, v13, vcc
	global_load_dwordx4 v[28:31], v[8:9], off
	ds_read_b128 v[8:11], v11
	s_mov_b32 s4, 0x800000
	s_lshl_b64 s[0:1], s[2:3], 12
	s_add_u32 s0, s8, s0
	s_addc_u32 s1, s9, s1
	s_waitcnt lgkmcnt(0)
	v_add_f32_e32 v8, v8, v9
	v_add_f32_e32 v8, v8, v10
	v_add_f32_e32 v8, v8, v11
	v_fmac_f32_e32 v12, 0x3a000000, v8
	v_mul_f32_e32 v8, 0x4b800000, v12
	v_cmp_gt_f32_e32 vcc, s4, v12
	v_lshlrev_b32_e32 v9, 1, v14
	s_nop 0
	v_cndmask_b32_e32 v8, v12, v8, vcc
	v_rsq_f32_e32 v8, v8
	s_nop 0
	v_mul_f32_e32 v10, 0x45800000, v8
	v_cndmask_b32_e32 v8, v8, v10, vcc
	v_pk_mul_f32 v[0:1], v[8:9], v[0:1] op_sel_hi:[0,1]
	v_pk_mul_f32 v[2:3], v[8:9], v[2:3] op_sel_hi:[0,1]
	v_pk_mul_f32 v[4:5], v[8:9], v[4:5] op_sel_hi:[0,1]
	v_pk_mul_f32 v[6:7], v[8:9], v[6:7] op_sel_hi:[0,1]
	s_waitcnt vmcnt(2)
	v_pk_fma_f32 v[0:1], v[16:17], v[0:1], v[20:21]
	v_pk_fma_f32 v[2:3], v[18:19], v[2:3], v[22:23]
	v_cvt_pk_f16_f32 v0, v0, v1
	v_cvt_pk_f16_f32 v1, v2, v3
	global_store_dwordx2 v9, v[0:1], s[0:1] sc1
	s_waitcnt vmcnt(1)
	v_pk_fma_f32 v[0:1], v[24:25], v[4:5], v[28:29]
	v_pk_fma_f32 v[2:3], v[26:27], v[6:7], v[30:31]
	v_cvt_pk_f16_f32 v0, v0, v1
	v_cvt_pk_f16_f32 v1, v2, v3
	global_store_dwordx2 v9, v[0:1], s[0:1] offset:2048 sc1
